# speedup vs baseline: 1.0140x; 1.0140x over previous
_Z12scan2_kernelPKDF16_S0_S0_S0_S0_PKfS2_S2_S2_PDF16_PfS4_:
	s_and_b32 s3, s2, 7
	s_lshr_b32 s2, s2, 3
	s_lshl_b32 s3, s3, 5
	s_or_b32 s2, s2, s3
	s_load_dwordx8 s[4:11], s[0:1], 0x0
	s_load_dwordx8 s[12:19], s[0:1], 0x20
	s_load_dwordx4 s[20:23], s[0:1], 0x40
	s_load_dwordx2 s[24:25], s[0:1], 0x50
	s_and_b32 s26, s2, 3
	s_bfe_u32 s27, s2, 0x50002
	s_lshr_b32 s28, s2, 7
	s_lshl_b32 s29, s26, 3
	v_lshrrev_b32_e32 v1, 6, v0
	v_and_b32_e32 v2, 15, v0
	v_bfe_u32 v3, v0, 4, 2
	v_and_b32_e32 v42, 63, v0
	v_readfirstlane_b32 s40, v1
	v_mov_b32_e32 v43, v0
	v_lshrrev_b32_e32 v14, 4, v43
	v_and_b32_e32 v15, 15, v43
	v_and_b32_e32 v188, 15, v14
	v_xor_b32_e32 v15, v15, v188
	v_lshlrev_b32_e32 v15, 4, v15
	v_lshl_or_b32 v4, v14, 13, v15
	v_lshl_or_b32 v6, v14, 8, v15
	v_lshrrev_b32_e32 v14, 3, v43
	v_and_b32_e32 v15, 7, v43
	v_and_b32_e32 v188, 7, v14
	v_xor_b32_e32 v15, v15, v188
	v_lshlrev_b32_e32 v15, 4, v15
	v_lshl_or_b32 v8, v14, 12, v15
	v_lshlrev_b32_e32 v40, 4, v43
	v_add_u32_e32 v32, 0xc800, v40
	v_add_u32_e32 v34, 0x19000, v40
	v_add_u32_e32 v43, 0x200, v0
	v_lshrrev_b32_e32 v14, 4, v43
	v_and_b32_e32 v15, 15, v43
	v_and_b32_e32 v188, 15, v14
	v_xor_b32_e32 v15, v15, v188
	v_lshlrev_b32_e32 v15, 4, v15
	v_lshl_or_b32 v5, v14, 13, v15
	v_lshl_or_b32 v7, v14, 8, v15
	v_lshrrev_b32_e32 v14, 3, v43
	v_and_b32_e32 v15, 7, v43
	v_and_b32_e32 v188, 7, v14
	v_xor_b32_e32 v15, v15, v188
	v_lshlrev_b32_e32 v15, 4, v15
	v_lshl_or_b32 v9, v14, 12, v15
	v_lshlrev_b32_e32 v41, 4, v43
	v_add_u32_e32 v33, 0xc800, v41
	v_add_u32_e32 v35, 0x19000, v41
	s_sub_u32 s45, 11, s40
	s_cmp_lt_u32 s40, 4
	s_cselect_b32 s41, s40, s45
	s_lshr_b32 s42, s41, 1
	s_lshl_b32 s43, s40, 10
	s_lshl_b32 s44, s40, 8
	s_and_b32 s45, s40, 1
	s_lshl_b32 s45, s45, 8
	v_lshl_add_u32 v10, v42, 2, s45
	s_lshl_b32 s45, s41, 4
	v_add_u32_e32 v14, s45, v2
	v_add_u32_e32 v15, 0, v3
	v_xor_b32_e32 v15, v15, v2
	v_lshlrev_b32_e32 v15, 4, v15
	v_lshl_or_b32 v16, v2, 8, v15
	v_add_u32_e32 v20, 0xc800, v16
	v_add_u32_e32 v212, 0x19000, v16
	v_add_u32_e32 v15, 4, v3
	v_xor_b32_e32 v15, v15, v2
	v_lshlrev_b32_e32 v15, 4, v15
	v_lshl_or_b32 v17, v2, 8, v15
	v_add_u32_e32 v21, 0xc800, v17
	v_add_u32_e32 v213, 0x19000, v17
	v_add_u32_e32 v15, 8, v3
	v_xor_b32_e32 v15, v15, v2
	v_lshlrev_b32_e32 v15, 4, v15
	v_lshl_or_b32 v18, v2, 8, v15
	v_add_u32_e32 v22, 0xc800, v18
	v_add_u32_e32 v214, 0x19000, v18
	v_add_u32_e32 v15, 12, v3
	v_xor_b32_e32 v15, v15, v2
	v_lshlrev_b32_e32 v15, 4, v15
	v_lshl_or_b32 v19, v2, 8, v15
	v_add_u32_e32 v23, 0xc800, v19
	v_add_u32_e32 v215, 0x19000, v19
	v_lshrrev_b32_e32 v188, 1, v3
	v_and_b32_e32 v189, 7, v14
	v_and_b32_e32 v190, 1, v3
	v_lshlrev_b32_e32 v190, 3, v190
	v_lshl_or_b32 v190, v14, 7, v190
	v_add_u32_e32 v15, 0, v188
	v_xor_b32_e32 v15, v15, v189
	v_lshl_add_u32 v24, v15, 4, v190
	v_add_u32_e32 v28, 0xc800, v24
	v_add_u32_e32 v216, 0x19000, v24
	v_add_u32_e32 v15, 2, v188
	v_xor_b32_e32 v15, v15, v189
	v_lshl_add_u32 v25, v15, 4, v190
	v_add_u32_e32 v29, 0xc800, v25
	v_add_u32_e32 v217, 0x19000, v25
	v_add_u32_e32 v15, 4, v188
	v_xor_b32_e32 v15, v15, v189
	v_lshl_add_u32 v26, v15, 4, v190
	v_add_u32_e32 v30, 0xc800, v26
	v_add_u32_e32 v218, 0x19000, v26
	v_add_u32_e32 v15, 6, v188
	v_xor_b32_e32 v15, v15, v189
	v_lshl_add_u32 v27, v15, 4, v190
	v_add_u32_e32 v31, 0xc800, v27
	v_add_u32_e32 v219, 0x19000, v27
	v_lshlrev_b32_e32 v242, 12, v14
	v_lshl_add_u32 v242, v3, 3, v242
	v_lshlrev_b32_e32 v36, 2, v14
	v_add_u32_e32 v37, 0xc800, v36
	v_add_u32_e32 v220, 0x19000, v36
	v_lshlrev_b32_e32 v38, 5, v3
	v_add_u32_e32 v39, 0xc800, v38
	v_add_u32_e32 v221, 0x19000, v38
	s_and_b32 s45, s41, 1
	s_lshl_b32 s45, s45, 4
	v_add_u32_e32 v43, s45, v2
	v_lshlrev_b32_e32 v189, 3, v3
	v_sub_u32_e32 v43, v43, v189
	v_cmp_le_i32_e64 s[52:53], 0, v43
	v_cmp_le_i32_e64 s[54:55], 1, v43
	v_cmp_le_i32_e64 s[56:57], 2, v43
	v_cmp_le_i32_e64 s[58:59], 3, v43
	v_cmp_le_i32_e64 s[60:61], 4, v43
	v_cmp_le_i32_e64 s[62:63], 5, v43
	v_cmp_le_i32_e64 s[64:65], 6, v43
	v_cmp_le_i32_e64 s[66:67], 7, v43
	v_cmp_eq_u32_e32 vcc, 0, v43
	s_nop 1
	v_cndmask_b32_e64 v188, 0, 1.0, vcc
	v_cmp_eq_u32_e32 vcc, 1, v43
	s_nop 1
	v_cndmask_b32_e64 v189, 0, 1.0, vcc
	v_cmp_eq_u32_e32 vcc, 2, v43
	s_nop 1
	v_cndmask_b32_e64 v190, 0, 1.0, vcc
	v_cmp_eq_u32_e32 vcc, 3, v43
	s_nop 1
	v_cndmask_b32_e64 v191, 0, 1.0, vcc
	v_cmp_eq_u32_e32 vcc, 4, v43
	s_nop 1
	v_cndmask_b32_e64 v192, 0, 1.0, vcc
	v_cmp_eq_u32_e32 vcc, 5, v43
	s_nop 1
	v_cndmask_b32_e64 v193, 0, 1.0, vcc
	v_cmp_eq_u32_e32 vcc, 6, v43
	s_nop 1
	v_cndmask_b32_e64 v194, 0, 1.0, vcc
	v_cmp_eq_u32_e32 vcc, 7, v43
	s_nop 1
	v_cndmask_b32_e64 v195, 0, 1.0, vcc
	v_cvt_pk_f16_f32 v92, v188, v189
	v_cvt_pk_f16_f32 v93, v190, v191
	v_cvt_pk_f16_f32 v94, v192, v193
	v_cvt_pk_f16_f32 v95, v194, v195
	v_mov_b32_e32 v250, 0
	v_mov_b32_e32 v251, 0
	s_waitcnt lgkmcnt(0)
	s_lshl_b32 s45, s28, 12
	s_lshl_b32 s48, s27, 7
	s_add_u32 s45, s45, s48
	s_lshl_b32 s48, s45, 9
	s_add_u32 s48, s4, s48
	s_addc_u32 s49, s5, 0
	v_lshlrev_b32_e32 v188, 9, v14
	v_lshl_add_u32 v188, v3, 4, v188
	global_load_dwordx4 v[44:47], v188, s[48:49] offset:256
	global_load_dwordx4 v[48:51], v188, s[48:49] offset:320
	global_load_dwordx4 v[52:55], v188, s[48:49] offset:384
	global_load_dwordx4 v[56:59], v188, s[48:49] offset:448
	s_lshl_b32 s48, s28, 5
	s_add_u32 s48, s48, s27
	s_lshl_b32 s48, s48, 15
	s_add_u32 s48, s10, s48
	s_addc_u32 s49, s11, 0
	v_lshlrev_b32_e32 v188, 8, v14
	v_lshl_add_u32 v188, v3, 4, v188
	global_load_dwordx4 v[144:147], v188, s[48:49] offset:0
	global_load_dwordx4 v[148:151], v188, s[48:49] offset:64
	global_load_dwordx4 v[152:155], v188, s[48:49] offset:128
	global_load_dwordx4 v[156:159], v188, s[48:49] offset:192
	v_and_b32_e32 v188, 7, v42
	v_add_u32_e32 v188, s29, v188
	v_lshlrev_b32_e32 v188, 2, v188
	global_load_dword v11, v188, s[20:21]
	global_load_dword v12, v188, s[18:19]
	s_mul_i32 s48, s28, 0x900
	s_lshl_b32 s49, s29, 6
	s_add_u32 s48, s48, s49
	s_lshl_b32 s48, s48, 13
	s_lshl_b32 s49, s27, 8
	s_add_u32 s48, s48, s49
	s_add_u32 s30, s6, s48
	s_addc_u32 s31, s7, 0
	s_lshl_b32 s48, s28, 5
	s_add_u32 s48, s48, s27
	s_lshl_b32 s48, s48, 5
	s_add_u32 s48, s48, s29
	s_lshl_b32 s48, s48, 14
	s_add_u32 s32, s12, s48
	s_addc_u32 s33, s13, 0
	s_lshl_b32 s48, s45, 12
	s_lshl_b32 s49, s29, 7
	s_add_u32 s48, s48, s49
	s_add_u32 s34, s8, s48
	s_addc_u32 s35, s9, 0
	s_add_u32 s38, s22, s48
	s_addc_u32 s39, s23, 0
	s_lshl_b32 s48, s28, 5
	s_add_u32 s48, s48, s29
	s_lshl_b32 s48, s48, 14
	s_lshl_b32 s49, s27, 9
	s_add_u32 s48, s48, s49
	s_lshr_b32 s49, s40, 1
	s_cmp_eq_u32 s49, 1
	s_cselect_b32 s50, s14, s16
	s_cselect_b32 s51, s15, s17
	s_add_u32 s36, s50, s48
	s_addc_u32 s37, s51, 0
	s_lshl_b32 s48, s45, 2
	s_add_u32 s24, s24, s48
	s_addc_u32 s25, s25, 0
	v_lshlrev_b32_e32 v15, 2, v14
	s_mov_b32 s51, 0xbfb8aa3b
	s_mov_b32 s50, 0x41800000
	s_add_u32 m0, s43, 0x0
	s_nop 0
	global_load_lds_dwordx4 v4, s[30:31]
	s_add_u32 m0, s43, 0x4000
	s_nop 0
	global_load_lds_dwordx4 v6, s[32:33]
	s_add_u32 m0, s43, 0x8000
	s_nop 0
	global_load_lds_dwordx4 v8, s[34:35]
	s_add_u32 m0, s43, 0x2000
	s_nop 0
	global_load_lds_dwordx4 v5, s[30:31]
	s_add_u32 m0, s43, 0x6000
	s_nop 0
	global_load_lds_dwordx4 v7, s[32:33]
	s_add_u32 m0, s43, 0xa000
	s_nop 0
	global_load_lds_dwordx4 v9, s[34:35]
	s_add_u32 m0, s44, 0xc000
	s_nop 0
	global_load_lds_dword v10, s[36:37]
	s_add_u32 s30, s30, 0x80000
	s_addc_u32 s31, s31, 0
	s_add_u32 s32, s32, 0x4000
	s_addc_u32 s33, s33, 0
	s_add_u32 s34, s34, 0x80
	s_addc_u32 s35, s35, 0
	s_add_u32 s36, s36, 0x4000
	s_addc_u32 s37, s37, 0
	s_add_u32 m0, s43, 0xc800
	s_nop 0
	global_load_lds_dwordx4 v4, s[30:31]
	s_add_u32 m0, s43, 0x10800
	s_nop 0
	global_load_lds_dwordx4 v6, s[32:33]
	s_add_u32 m0, s43, 0x14800
	s_nop 0
	global_load_lds_dwordx4 v8, s[34:35]
	s_add_u32 m0, s43, 0xe800
	s_nop 0
	global_load_lds_dwordx4 v5, s[30:31]
	s_add_u32 m0, s43, 0x12800
	s_nop 0
	global_load_lds_dwordx4 v7, s[32:33]
	s_add_u32 m0, s43, 0x16800
	s_nop 0
	global_load_lds_dwordx4 v9, s[34:35]
	s_add_u32 m0, s44, 0x18800
	s_nop 0
	global_load_lds_dword v10, s[36:37]
	s_add_u32 s30, s30, 0x80000
	s_addc_u32 s31, s31, 0
	s_add_u32 s32, s32, 0x4000
	s_addc_u32 s33, s33, 0
	s_add_u32 s34, s34, 0x80
	s_addc_u32 s35, s35, 0
	s_add_u32 s36, s36, 0x4000
	s_addc_u32 s37, s37, 0
	s_waitcnt vmcnt(19)
	v_cvt_f32_f16_e32 v60, v144
	v_cvt_f32_f16_sdwa v61, v144 dst_sel:DWORD dst_unused:UNUSED_PAD src0_sel:WORD_1
	v_cvt_f32_f16_e32 v62, v145
	v_cvt_f32_f16_sdwa v63, v145 dst_sel:DWORD dst_unused:UNUSED_PAD src0_sel:WORD_1
	v_cvt_f32_f16_e32 v64, v146
	v_cvt_f32_f16_sdwa v65, v146 dst_sel:DWORD dst_unused:UNUSED_PAD src0_sel:WORD_1
	v_cvt_f32_f16_e32 v66, v147
	v_cvt_f32_f16_sdwa v67, v147 dst_sel:DWORD dst_unused:UNUSED_PAD src0_sel:WORD_1
	s_waitcnt vmcnt(18)
	v_cvt_f32_f16_e32 v68, v148
	v_cvt_f32_f16_sdwa v69, v148 dst_sel:DWORD dst_unused:UNUSED_PAD src0_sel:WORD_1
	v_cvt_f32_f16_e32 v70, v149
	v_cvt_f32_f16_sdwa v71, v149 dst_sel:DWORD dst_unused:UNUSED_PAD src0_sel:WORD_1
	v_cvt_f32_f16_e32 v72, v150
	v_cvt_f32_f16_sdwa v73, v150 dst_sel:DWORD dst_unused:UNUSED_PAD src0_sel:WORD_1
	v_cvt_f32_f16_e32 v74, v151
	v_cvt_f32_f16_sdwa v75, v151 dst_sel:DWORD dst_unused:UNUSED_PAD src0_sel:WORD_1
	s_waitcnt vmcnt(17)
	v_cvt_f32_f16_e32 v76, v152
	v_cvt_f32_f16_sdwa v77, v152 dst_sel:DWORD dst_unused:UNUSED_PAD src0_sel:WORD_1
	v_cvt_f32_f16_e32 v78, v153
	v_cvt_f32_f16_sdwa v79, v153 dst_sel:DWORD dst_unused:UNUSED_PAD src0_sel:WORD_1
	v_cvt_f32_f16_e32 v80, v154
	v_cvt_f32_f16_sdwa v81, v154 dst_sel:DWORD dst_unused:UNUSED_PAD src0_sel:WORD_1
	v_cvt_f32_f16_e32 v82, v155
	v_cvt_f32_f16_sdwa v83, v155 dst_sel:DWORD dst_unused:UNUSED_PAD src0_sel:WORD_1
	s_waitcnt vmcnt(16)
	v_cvt_f32_f16_e32 v84, v156
	v_cvt_f32_f16_sdwa v85, v156 dst_sel:DWORD dst_unused:UNUSED_PAD src0_sel:WORD_1
	v_cvt_f32_f16_e32 v86, v157
	v_cvt_f32_f16_sdwa v87, v157 dst_sel:DWORD dst_unused:UNUSED_PAD src0_sel:WORD_1
	v_cvt_f32_f16_e32 v88, v158
	v_cvt_f32_f16_sdwa v89, v158 dst_sel:DWORD dst_unused:UNUSED_PAD src0_sel:WORD_1
	v_cvt_f32_f16_e32 v90, v159
	v_cvt_f32_f16_sdwa v91, v159 dst_sel:DWORD dst_unused:UNUSED_PAD src0_sel:WORD_1
	s_waitcnt vmcnt(14)
	s_waitcnt vmcnt(15)
	v_mul_f32_e32 v11, 0x41800000, v11
	s_waitcnt vmcnt(7)
	s_waitcnt lgkmcnt(0)
	s_barrier
	ds_read_b128 v[144:147], v16 offset:16384
	ds_read_b128 v[148:151], v16 offset:20480
	ds_read_b128 v[152:155], v16 offset:24576
	ds_read_b128 v[156:159], v16 offset:28672
	ds_read_b32 v189, v36 offset:49152
	s_add_u32 m0, s43, 0x19000
	s_nop 0
	global_load_lds_dwordx4 v4, s[30:31]
	s_add_u32 m0, s43, 0x1d000
	s_nop 0
	global_load_lds_dwordx4 v6, s[32:33]
	s_add_u32 m0, s43, 0x21000
	s_nop 0
	global_load_lds_dwordx4 v8, s[34:35]
	s_add_u32 m0, s43, 0x1b000
	s_nop 0
	global_load_lds_dwordx4 v5, s[30:31]
	s_add_u32 m0, s43, 0x1f000
	s_nop 0
	global_load_lds_dwordx4 v7, s[32:33]
	s_add_u32 m0, s43, 0x23000
	s_nop 0
	global_load_lds_dwordx4 v9, s[34:35]
	s_add_u32 m0, s44, 0x25000
	s_nop 0
	global_load_lds_dword v10, s[36:37]
	s_add_u32 s30, s30, 0x80000
	s_addc_u32 s31, s31, 0
	s_add_u32 s32, s32, 0x4000
	s_addc_u32 s33, s33, 0
	s_add_u32 s34, s34, 0x80
	s_addc_u32 s35, s35, 0
	s_add_u32 s36, s36, 0x4000
	s_addc_u32 s37, s37, 0
	ds_read_b128 v[160:163], v17 offset:16384
	ds_read_b128 v[164:167], v17 offset:20480
	ds_read_b128 v[168:171], v17 offset:24576
	ds_read_b128 v[172:175], v17 offset:28672
	s_waitcnt lgkmcnt(4)
	v_mfma_f32_16x16x32_f16 v[96:99], v[144:147], v[44:47], 0
	v_mfma_f32_16x16x32_f16 v[100:103], v[148:151], v[44:47], 0
	v_mfma_f32_16x16x32_f16 v[104:107], v[152:155], v[44:47], 0
	v_mfma_f32_16x16x32_f16 v[108:111], v[156:159], v[44:47], 0
	ds_read_b128 v[144:147], v18 offset:16384
	ds_read_b128 v[148:151], v18 offset:20480
	ds_read_b128 v[152:155], v18 offset:24576
	ds_read_b128 v[156:159], v18 offset:28672
	s_waitcnt lgkmcnt(4)
	v_mfma_f32_16x16x32_f16 v[96:99], v[160:163], v[48:51], v[96:99]
	v_mfma_f32_16x16x32_f16 v[100:103], v[164:167], v[48:51], v[100:103]
	v_mfma_f32_16x16x32_f16 v[104:107], v[168:171], v[48:51], v[104:107]
	v_mfma_f32_16x16x32_f16 v[108:111], v[172:175], v[48:51], v[108:111]
	ds_read_b128 v[160:163], v19 offset:16384
	ds_read_b128 v[164:167], v19 offset:20480
	ds_read_b128 v[168:171], v19 offset:24576
	ds_read_b128 v[172:175], v19 offset:28672
	s_waitcnt lgkmcnt(4)
	v_mfma_f32_16x16x32_f16 v[96:99], v[144:147], v[52:55], v[96:99]
	v_mfma_f32_16x16x32_f16 v[100:103], v[148:151], v[52:55], v[100:103]
	v_mfma_f32_16x16x32_f16 v[104:107], v[152:155], v[52:55], v[104:107]
	v_mfma_f32_16x16x32_f16 v[108:111], v[156:159], v[52:55], v[108:111]
	ds_read_b128 v[176:179], v38 offset:49664
	ds_read_b128 v[180:183], v38 offset:49680
	ds_read_b32 v188, v38 offset:49152
	ds_read_b128 v[144:147], v16 offset:0
	ds_read_b128 v[148:151], v16 offset:4096
	ds_read_b128 v[152:155], v16 offset:8192
	ds_read_b128 v[156:159], v16 offset:12288
	s_waitcnt lgkmcnt(7)
	v_mfma_f32_16x16x32_f16 v[96:99], v[160:163], v[56:59], v[96:99]
	v_mfma_f32_16x16x32_f16 v[100:103], v[164:167], v[56:59], v[100:103]
	v_mfma_f32_16x16x32_f16 v[104:107], v[168:171], v[56:59], v[104:107]
	v_mfma_f32_16x16x32_f16 v[108:111], v[172:175], v[56:59], v[108:111]
	v_mul_f32_e32 v189, 0x3fb8aa3b, v189
	s_cmp_lt_u32 s42, 0
	s_cbranch_scc1 .Lmy_s2_kend1
	s_cmp_eq_u32 s42, 0
	s_cbranch_scc1 .Lmy_s2_diag2
	ds_read_b128 v[224:227], v38 offset:49792
	ds_read_b128 v[228:231], v38 offset:49808
	ds_read_b32 v232, v38 offset:49280
	ds_read_b128 v[160:163], v17 offset:0
	ds_read_b128 v[164:167], v17 offset:4096
	ds_read_b128 v[168:171], v17 offset:8192
	ds_read_b128 v[172:175], v17 offset:12288
	s_waitcnt lgkmcnt(7)
	v_fma_f32 v188, v188, s51, v189
	v_exp_f32_e32 v188, v188
	s_nop 0
	v_pk_mul_f32 v[176:177], v[176:177], v[188:189] op_sel_hi:[1,0]
	v_pk_mul_f32 v[178:179], v[178:179], v[188:189] op_sel_hi:[1,0]
	v_pk_mul_f32 v[180:181], v[180:181], v[188:189] op_sel_hi:[1,0]
	v_pk_mul_f32 v[182:183], v[182:183], v[188:189] op_sel_hi:[1,0]
	v_pk_mul_f32 v[176:177], v[60:61], v[176:177]
	v_pk_mul_f32 v[178:179], v[62:63], v[178:179]
	v_pk_mul_f32 v[180:181], v[64:65], v[180:181]
	v_pk_mul_f32 v[182:183], v[66:67], v[182:183]
	v_cvt_pk_f16_f32 v184, v176, v177
	v_cvt_pk_f16_f32 v185, v178, v179
	v_cvt_pk_f16_f32 v186, v180, v181
	v_cvt_pk_f16_f32 v187, v182, v183
	s_nop 1
	v_mfma_f32_16x16x32_f16 v[112:115], v[144:147], v[184:187], 0
	v_mfma_f32_16x16x32_f16 v[116:119], v[148:151], v[184:187], 0
	v_mfma_f32_16x16x32_f16 v[120:123], v[152:155], v[184:187], 0
	v_mfma_f32_16x16x32_f16 v[124:127], v[156:159], v[184:187], 0
	s_branch .Lmy_s2_knext3
.Lmy_s2_diag2:
	ds_read_b64 v[234:235], v24 offset:32768
	ds_read_b64 v[236:237], v25 offset:32768
	ds_read_b64 v[238:239], v26 offset:32768
	ds_read_b64 v[240:241], v27 offset:32768
	s_waitcnt lgkmcnt(4)
	v_fma_f32 v188, v188, s51, v189
	v_exp_f32_e32 v188, v188
	s_nop 0
	v_pk_mul_f32 v[176:177], v[176:177], v[188:189] op_sel_hi:[1,0]
	v_pk_mul_f32 v[178:179], v[178:179], v[188:189] op_sel_hi:[1,0]
	v_pk_mul_f32 v[180:181], v[180:181], v[188:189] op_sel_hi:[1,0]
	v_pk_mul_f32 v[182:183], v[182:183], v[188:189] op_sel_hi:[1,0]
	v_pk_mul_f32 v[176:177], v[60:61], v[176:177]
	v_pk_mul_f32 v[178:179], v[62:63], v[178:179]
	v_pk_mul_f32 v[180:181], v[64:65], v[180:181]
	v_pk_mul_f32 v[182:183], v[66:67], v[182:183]
	v_cndmask_b32_e64 v176, 0, v176, s[52:53]
	v_cndmask_b32_e64 v177, 0, v177, s[54:55]
	v_cndmask_b32_e64 v178, 0, v178, s[56:57]
	v_cndmask_b32_e64 v179, 0, v179, s[58:59]
	v_cndmask_b32_e64 v180, 0, v180, s[60:61]
	v_cndmask_b32_e64 v181, 0, v181, s[62:63]
	v_cndmask_b32_e64 v182, 0, v182, s[64:65]
	v_cndmask_b32_e64 v183, 0, v183, s[66:67]
	v_cvt_pk_f16_f32 v184, v176, v177
	v_cvt_pk_f16_f32 v185, v178, v179
	v_cvt_pk_f16_f32 v186, v180, v181
	v_cvt_pk_f16_f32 v187, v182, v183
	s_nop 1
	v_mfma_f32_16x16x32_f16 v[112:115], v[144:147], v[184:187], 0
	v_mfma_f32_16x16x32_f16 v[116:119], v[148:151], v[184:187], 0
	v_mfma_f32_16x16x32_f16 v[120:123], v[152:155], v[184:187], 0
	v_mfma_f32_16x16x32_f16 v[124:127], v[156:159], v[184:187], 0
	v_mfma_f32_16x16x32_f16 v[128:131], v[144:147], v[92:95], 0
	v_mfma_f32_16x16x32_f16 v[132:135], v[148:151], v[92:95], 0
	v_mfma_f32_16x16x32_f16 v[136:139], v[152:155], v[92:95], 0
	v_mfma_f32_16x16x32_f16 v[140:143], v[156:159], v[92:95], 0
	s_branch .Lmy_s2_kend1
.Lmy_s2_knext3:
	s_cmp_lt_u32 s42, 1
	s_cbranch_scc1 .Lmy_s2_kend1
	s_cmp_eq_u32 s42, 1
	s_cbranch_scc1 .Lmy_s2_diag4
	ds_read_b128 v[176:179], v38 offset:49920
	ds_read_b128 v[180:183], v38 offset:49936
	ds_read_b32 v188, v38 offset:49408
	ds_read_b128 v[144:147], v18 offset:0
	ds_read_b128 v[148:151], v18 offset:4096
	ds_read_b128 v[152:155], v18 offset:8192
	ds_read_b128 v[156:159], v18 offset:12288
	s_waitcnt lgkmcnt(7)
	v_fma_f32 v232, v232, s51, v189
	v_exp_f32_e32 v232, v232
	s_nop 0
	v_pk_mul_f32 v[224:225], v[224:225], v[232:233] op_sel_hi:[1,0]
	v_pk_mul_f32 v[226:227], v[226:227], v[232:233] op_sel_hi:[1,0]
	v_pk_mul_f32 v[228:229], v[228:229], v[232:233] op_sel_hi:[1,0]
	v_pk_mul_f32 v[230:231], v[230:231], v[232:233] op_sel_hi:[1,0]
	v_pk_mul_f32 v[224:225], v[68:69], v[224:225]
	v_pk_mul_f32 v[226:227], v[70:71], v[226:227]
	v_pk_mul_f32 v[228:229], v[72:73], v[228:229]
	v_pk_mul_f32 v[230:231], v[74:75], v[230:231]
	v_cvt_pk_f16_f32 v184, v224, v225
	v_cvt_pk_f16_f32 v185, v226, v227
	v_cvt_pk_f16_f32 v186, v228, v229
	v_cvt_pk_f16_f32 v187, v230, v231
	s_nop 1
	v_mfma_f32_16x16x32_f16 v[112:115], v[160:163], v[184:187], v[112:115]
	v_mfma_f32_16x16x32_f16 v[116:119], v[164:167], v[184:187], v[116:119]
	v_mfma_f32_16x16x32_f16 v[120:123], v[168:171], v[184:187], v[120:123]
	v_mfma_f32_16x16x32_f16 v[124:127], v[172:175], v[184:187], v[124:127]
	s_branch .Lmy_s2_knext5
.Lmy_s2_diag4:
	ds_read_b64 v[234:235], v24 offset:32768
	ds_read_b64 v[236:237], v25 offset:32768
	ds_read_b64 v[238:239], v26 offset:32768
	ds_read_b64 v[240:241], v27 offset:32768
	s_waitcnt lgkmcnt(4)
	v_fma_f32 v232, v232, s51, v189
	v_exp_f32_e32 v232, v232
	s_nop 0
	v_pk_mul_f32 v[224:225], v[224:225], v[232:233] op_sel_hi:[1,0]
	v_pk_mul_f32 v[226:227], v[226:227], v[232:233] op_sel_hi:[1,0]
	v_pk_mul_f32 v[228:229], v[228:229], v[232:233] op_sel_hi:[1,0]
	v_pk_mul_f32 v[230:231], v[230:231], v[232:233] op_sel_hi:[1,0]
	v_pk_mul_f32 v[224:225], v[68:69], v[224:225]
	v_pk_mul_f32 v[226:227], v[70:71], v[226:227]
	v_pk_mul_f32 v[228:229], v[72:73], v[228:229]
	v_pk_mul_f32 v[230:231], v[74:75], v[230:231]
	v_cndmask_b32_e64 v224, 0, v224, s[52:53]
	v_cndmask_b32_e64 v225, 0, v225, s[54:55]
	v_cndmask_b32_e64 v226, 0, v226, s[56:57]
	v_cndmask_b32_e64 v227, 0, v227, s[58:59]
	v_cndmask_b32_e64 v228, 0, v228, s[60:61]
	v_cndmask_b32_e64 v229, 0, v229, s[62:63]
	v_cndmask_b32_e64 v230, 0, v230, s[64:65]
	v_cndmask_b32_e64 v231, 0, v231, s[66:67]
	v_cvt_pk_f16_f32 v184, v224, v225
	v_cvt_pk_f16_f32 v185, v226, v227
	v_cvt_pk_f16_f32 v186, v228, v229
	v_cvt_pk_f16_f32 v187, v230, v231
	s_nop 1
	v_mfma_f32_16x16x32_f16 v[112:115], v[160:163], v[184:187], v[112:115]
	v_mfma_f32_16x16x32_f16 v[116:119], v[164:167], v[184:187], v[116:119]
	v_mfma_f32_16x16x32_f16 v[120:123], v[168:171], v[184:187], v[120:123]
	v_mfma_f32_16x16x32_f16 v[124:127], v[172:175], v[184:187], v[124:127]
	v_mfma_f32_16x16x32_f16 v[128:131], v[160:163], v[92:95], 0
	v_mfma_f32_16x16x32_f16 v[132:135], v[164:167], v[92:95], 0
	v_mfma_f32_16x16x32_f16 v[136:139], v[168:171], v[92:95], 0
	v_mfma_f32_16x16x32_f16 v[140:143], v[172:175], v[92:95], 0
	s_branch .Lmy_s2_kend1
.Lmy_s2_knext5:
	s_cmp_lt_u32 s42, 2
	s_cbranch_scc1 .Lmy_s2_kend1
	s_cmp_eq_u32 s42, 2
	s_cbranch_scc1 .Lmy_s2_diag6
	ds_read_b128 v[224:227], v38 offset:50048
	ds_read_b128 v[228:231], v38 offset:50064
	ds_read_b32 v232, v38 offset:49536
	ds_read_b128 v[160:163], v19 offset:0
	ds_read_b128 v[164:167], v19 offset:4096
	ds_read_b128 v[168:171], v19 offset:8192
	ds_read_b128 v[172:175], v19 offset:12288
	s_waitcnt lgkmcnt(7)
	v_fma_f32 v188, v188, s51, v189
	v_exp_f32_e32 v188, v188
	s_nop 0
	v_pk_mul_f32 v[176:177], v[176:177], v[188:189] op_sel_hi:[1,0]
	v_pk_mul_f32 v[178:179], v[178:179], v[188:189] op_sel_hi:[1,0]
	v_pk_mul_f32 v[180:181], v[180:181], v[188:189] op_sel_hi:[1,0]
	v_pk_mul_f32 v[182:183], v[182:183], v[188:189] op_sel_hi:[1,0]
	v_pk_mul_f32 v[176:177], v[76:77], v[176:177]
	v_pk_mul_f32 v[178:179], v[78:79], v[178:179]
	v_pk_mul_f32 v[180:181], v[80:81], v[180:181]
	v_pk_mul_f32 v[182:183], v[82:83], v[182:183]
	v_cvt_pk_f16_f32 v184, v176, v177
	v_cvt_pk_f16_f32 v185, v178, v179
	v_cvt_pk_f16_f32 v186, v180, v181
	v_cvt_pk_f16_f32 v187, v182, v183
	s_nop 1
	v_mfma_f32_16x16x32_f16 v[112:115], v[144:147], v[184:187], v[112:115]
	v_mfma_f32_16x16x32_f16 v[116:119], v[148:151], v[184:187], v[116:119]
	v_mfma_f32_16x16x32_f16 v[120:123], v[152:155], v[184:187], v[120:123]
	v_mfma_f32_16x16x32_f16 v[124:127], v[156:159], v[184:187], v[124:127]
	s_branch .Lmy_s2_knext7
.Lmy_s2_diag6:
	ds_read_b64 v[234:235], v24 offset:32768
	ds_read_b64 v[236:237], v25 offset:32768
	ds_read_b64 v[238:239], v26 offset:32768
	ds_read_b64 v[240:241], v27 offset:32768
	s_waitcnt lgkmcnt(4)
	v_fma_f32 v188, v188, s51, v189
	v_exp_f32_e32 v188, v188
	s_nop 0
	v_pk_mul_f32 v[176:177], v[176:177], v[188:189] op_sel_hi:[1,0]
	v_pk_mul_f32 v[178:179], v[178:179], v[188:189] op_sel_hi:[1,0]
	v_pk_mul_f32 v[180:181], v[180:181], v[188:189] op_sel_hi:[1,0]
	v_pk_mul_f32 v[182:183], v[182:183], v[188:189] op_sel_hi:[1,0]
	v_pk_mul_f32 v[176:177], v[76:77], v[176:177]
	v_pk_mul_f32 v[178:179], v[78:79], v[178:179]
	v_pk_mul_f32 v[180:181], v[80:81], v[180:181]
	v_pk_mul_f32 v[182:183], v[82:83], v[182:183]
	v_cndmask_b32_e64 v176, 0, v176, s[52:53]
	v_cndmask_b32_e64 v177, 0, v177, s[54:55]
	v_cndmask_b32_e64 v178, 0, v178, s[56:57]
	v_cndmask_b32_e64 v179, 0, v179, s[58:59]
	v_cndmask_b32_e64 v180, 0, v180, s[60:61]
	v_cndmask_b32_e64 v181, 0, v181, s[62:63]
	v_cndmask_b32_e64 v182, 0, v182, s[64:65]
	v_cndmask_b32_e64 v183, 0, v183, s[66:67]
	v_cvt_pk_f16_f32 v184, v176, v177
	v_cvt_pk_f16_f32 v185, v178, v179
	v_cvt_pk_f16_f32 v186, v180, v181
	v_cvt_pk_f16_f32 v187, v182, v183
	s_nop 1
	v_mfma_f32_16x16x32_f16 v[112:115], v[144:147], v[184:187], v[112:115]
	v_mfma_f32_16x16x32_f16 v[116:119], v[148:151], v[184:187], v[116:119]
	v_mfma_f32_16x16x32_f16 v[120:123], v[152:155], v[184:187], v[120:123]
	v_mfma_f32_16x16x32_f16 v[124:127], v[156:159], v[184:187], v[124:127]
	v_mfma_f32_16x16x32_f16 v[128:131], v[144:147], v[92:95], 0
	v_mfma_f32_16x16x32_f16 v[132:135], v[148:151], v[92:95], 0
	v_mfma_f32_16x16x32_f16 v[136:139], v[152:155], v[92:95], 0
	v_mfma_f32_16x16x32_f16 v[140:143], v[156:159], v[92:95], 0
	s_branch .Lmy_s2_kend1
.Lmy_s2_knext7:
	s_cmp_lt_u32 s42, 3
	s_cbranch_scc1 .Lmy_s2_kend1
	s_cmp_eq_u32 s42, 3
	s_cbranch_scc1 .Lmy_s2_diag8
	s_waitcnt lgkmcnt(0)
	v_fma_f32 v232, v232, s51, v189
	v_exp_f32_e32 v232, v232
	s_nop 0
	v_pk_mul_f32 v[224:225], v[224:225], v[232:233] op_sel_hi:[1,0]
	v_pk_mul_f32 v[226:227], v[226:227], v[232:233] op_sel_hi:[1,0]
	v_pk_mul_f32 v[228:229], v[228:229], v[232:233] op_sel_hi:[1,0]
	v_pk_mul_f32 v[230:231], v[230:231], v[232:233] op_sel_hi:[1,0]
	v_pk_mul_f32 v[224:225], v[84:85], v[224:225]
	v_pk_mul_f32 v[226:227], v[86:87], v[226:227]
	v_pk_mul_f32 v[228:229], v[88:89], v[228:229]
	v_pk_mul_f32 v[230:231], v[90:91], v[230:231]
	v_cvt_pk_f16_f32 v184, v224, v225
	v_cvt_pk_f16_f32 v185, v226, v227
	v_cvt_pk_f16_f32 v186, v228, v229
	v_cvt_pk_f16_f32 v187, v230, v231
	s_nop 1
	v_mfma_f32_16x16x32_f16 v[112:115], v[160:163], v[184:187], v[112:115]
	v_mfma_f32_16x16x32_f16 v[116:119], v[164:167], v[184:187], v[116:119]
	v_mfma_f32_16x16x32_f16 v[120:123], v[168:171], v[184:187], v[120:123]
	v_mfma_f32_16x16x32_f16 v[124:127], v[172:175], v[184:187], v[124:127]
	s_branch .Lmy_s2_knext9
.Lmy_s2_diag8:
	ds_read_b64 v[234:235], v24 offset:32768
	ds_read_b64 v[236:237], v25 offset:32768
	ds_read_b64 v[238:239], v26 offset:32768
	ds_read_b64 v[240:241], v27 offset:32768
	s_waitcnt lgkmcnt(4)
	v_fma_f32 v232, v232, s51, v189
	v_exp_f32_e32 v232, v232
	s_nop 0
	v_pk_mul_f32 v[224:225], v[224:225], v[232:233] op_sel_hi:[1,0]
	v_pk_mul_f32 v[226:227], v[226:227], v[232:233] op_sel_hi:[1,0]
	v_pk_mul_f32 v[228:229], v[228:229], v[232:233] op_sel_hi:[1,0]
	v_pk_mul_f32 v[230:231], v[230:231], v[232:233] op_sel_hi:[1,0]
	v_pk_mul_f32 v[224:225], v[84:85], v[224:225]
	v_pk_mul_f32 v[226:227], v[86:87], v[226:227]
	v_pk_mul_f32 v[228:229], v[88:89], v[228:229]
	v_pk_mul_f32 v[230:231], v[90:91], v[230:231]
	v_cndmask_b32_e64 v224, 0, v224, s[52:53]
	v_cndmask_b32_e64 v225, 0, v225, s[54:55]
	v_cndmask_b32_e64 v226, 0, v226, s[56:57]
	v_cndmask_b32_e64 v227, 0, v227, s[58:59]
	v_cndmask_b32_e64 v228, 0, v228, s[60:61]
	v_cndmask_b32_e64 v229, 0, v229, s[62:63]
	v_cndmask_b32_e64 v230, 0, v230, s[64:65]
	v_cndmask_b32_e64 v231, 0, v231, s[66:67]
	v_cvt_pk_f16_f32 v184, v224, v225
	v_cvt_pk_f16_f32 v185, v226, v227
	v_cvt_pk_f16_f32 v186, v228, v229
	v_cvt_pk_f16_f32 v187, v230, v231
	s_nop 1
	v_mfma_f32_16x16x32_f16 v[112:115], v[160:163], v[184:187], v[112:115]
	v_mfma_f32_16x16x32_f16 v[116:119], v[164:167], v[184:187], v[116:119]
	v_mfma_f32_16x16x32_f16 v[120:123], v[168:171], v[184:187], v[120:123]
	v_mfma_f32_16x16x32_f16 v[124:127], v[172:175], v[184:187], v[124:127]
	v_mfma_f32_16x16x32_f16 v[128:131], v[160:163], v[92:95], 0
	v_mfma_f32_16x16x32_f16 v[132:135], v[164:167], v[92:95], 0
	v_mfma_f32_16x16x32_f16 v[136:139], v[168:171], v[92:95], 0
	v_mfma_f32_16x16x32_f16 v[140:143], v[172:175], v[92:95], 0
	s_branch .Lmy_s2_kend1
.Lmy_s2_knext9:
.Lmy_s2_kend1:
	v_readlane_b32 s46, v11, 0
	v_readlane_b32 s47, v12, 0
	v_exp_f32_e32 v190, v189
	s_waitcnt lgkmcnt(0)
	s_nop 7
	v_cvt_f32_f16_e32 v198, v234
	v_cvt_f32_f16_sdwa v199, v234 dst_sel:DWORD dst_unused:UNUSED_PAD src0_sel:WORD_1
	v_cvt_f32_f16_e32 v200, v235
	v_cvt_f32_f16_sdwa v201, v235 dst_sel:DWORD dst_unused:UNUSED_PAD src0_sel:WORD_1
	v_pk_fma_f32 v[192:193], v[190:191], v[96:97], v[112:113] op_sel_hi:[0,1,1]
	v_pk_fma_f32 v[194:195], v[190:191], v[98:99], v[114:115] op_sel_hi:[0,1,1]
	v_pk_mul_f32 v[192:193], v[192:193], s[46:47] op_sel:[0,1] op_sel_hi:[1,1]
	v_pk_mul_f32 v[194:195], v[194:195], s[46:47] op_sel:[0,1] op_sel_hi:[1,1]
	v_pk_fma_f32 v[192:193], s[46:47], v[128:129], v[192:193] op_sel_hi:[0,1,1]
	v_pk_fma_f32 v[194:195], s[46:47], v[130:131], v[194:195] op_sel_hi:[0,1,1]
	v_pk_mul_f32 v[192:193], v[192:193], v[198:199]
	v_pk_mul_f32 v[194:195], v[194:195], v[200:201]
	v_pk_fma_f32 v[250:251], v[192:193], v[192:193], v[250:251]
	v_pk_fma_f32 v[250:251], v[194:195], v[194:195], v[250:251]
	v_cvt_pk_f16_f32 v196, v192, v193
	v_cvt_pk_f16_f32 v197, v194, v195
	global_store_dwordx2 v242, v[196:197], s[38:39]
	v_cvt_f32_f16_e32 v198, v236
	v_cvt_f32_f16_sdwa v199, v236 dst_sel:DWORD dst_unused:UNUSED_PAD src0_sel:WORD_1
	v_cvt_f32_f16_e32 v200, v237
	v_cvt_f32_f16_sdwa v201, v237 dst_sel:DWORD dst_unused:UNUSED_PAD src0_sel:WORD_1
	v_pk_fma_f32 v[192:193], v[190:191], v[100:101], v[116:117] op_sel_hi:[0,1,1]
	v_pk_fma_f32 v[194:195], v[190:191], v[102:103], v[118:119] op_sel_hi:[0,1,1]
	v_pk_mul_f32 v[192:193], v[192:193], s[46:47] op_sel:[0,1] op_sel_hi:[1,1]
	v_pk_mul_f32 v[194:195], v[194:195], s[46:47] op_sel:[0,1] op_sel_hi:[1,1]
	v_pk_fma_f32 v[192:193], s[46:47], v[132:133], v[192:193] op_sel_hi:[0,1,1]
	v_pk_fma_f32 v[194:195], s[46:47], v[134:135], v[194:195] op_sel_hi:[0,1,1]
	v_pk_mul_f32 v[192:193], v[192:193], v[198:199]
	v_pk_mul_f32 v[194:195], v[194:195], v[200:201]
	v_pk_fma_f32 v[250:251], v[192:193], v[192:193], v[250:251]
	v_pk_fma_f32 v[250:251], v[194:195], v[194:195], v[250:251]
	v_cvt_pk_f16_f32 v196, v192, v193
	v_cvt_pk_f16_f32 v197, v194, v195
	global_store_dwordx2 v242, v[196:197], s[38:39] offset:32
	v_cvt_f32_f16_e32 v198, v238
	v_cvt_f32_f16_sdwa v199, v238 dst_sel:DWORD dst_unused:UNUSED_PAD src0_sel:WORD_1
	v_cvt_f32_f16_e32 v200, v239
	v_cvt_f32_f16_sdwa v201, v239 dst_sel:DWORD dst_unused:UNUSED_PAD src0_sel:WORD_1
	v_pk_fma_f32 v[192:193], v[190:191], v[104:105], v[120:121] op_sel_hi:[0,1,1]
	v_pk_fma_f32 v[194:195], v[190:191], v[106:107], v[122:123] op_sel_hi:[0,1,1]
	v_pk_mul_f32 v[192:193], v[192:193], s[46:47] op_sel:[0,1] op_sel_hi:[1,1]
	v_pk_mul_f32 v[194:195], v[194:195], s[46:47] op_sel:[0,1] op_sel_hi:[1,1]
	v_pk_fma_f32 v[192:193], s[46:47], v[136:137], v[192:193] op_sel_hi:[0,1,1]
	v_pk_fma_f32 v[194:195], s[46:47], v[138:139], v[194:195] op_sel_hi:[0,1,1]
	v_pk_mul_f32 v[192:193], v[192:193], v[198:199]
	v_pk_mul_f32 v[194:195], v[194:195], v[200:201]
	v_pk_fma_f32 v[250:251], v[192:193], v[192:193], v[250:251]
	v_pk_fma_f32 v[250:251], v[194:195], v[194:195], v[250:251]
	v_cvt_pk_f16_f32 v196, v192, v193
	v_cvt_pk_f16_f32 v197, v194, v195
	global_store_dwordx2 v242, v[196:197], s[38:39] offset:64
	v_cvt_f32_f16_e32 v198, v240
	v_cvt_f32_f16_sdwa v199, v240 dst_sel:DWORD dst_unused:UNUSED_PAD src0_sel:WORD_1
	v_cvt_f32_f16_e32 v200, v241
	v_cvt_f32_f16_sdwa v201, v241 dst_sel:DWORD dst_unused:UNUSED_PAD src0_sel:WORD_1
	v_pk_fma_f32 v[192:193], v[190:191], v[108:109], v[124:125] op_sel_hi:[0,1,1]
	v_pk_fma_f32 v[194:195], v[190:191], v[110:111], v[126:127] op_sel_hi:[0,1,1]
	v_pk_mul_f32 v[192:193], v[192:193], s[46:47] op_sel:[0,1] op_sel_hi:[1,1]
	v_pk_mul_f32 v[194:195], v[194:195], s[46:47] op_sel:[0,1] op_sel_hi:[1,1]
	v_pk_fma_f32 v[192:193], s[46:47], v[140:141], v[192:193] op_sel_hi:[0,1,1]
	v_pk_fma_f32 v[194:195], s[46:47], v[142:143], v[194:195] op_sel_hi:[0,1,1]
	v_pk_mul_f32 v[192:193], v[192:193], v[198:199]
	v_pk_mul_f32 v[194:195], v[194:195], v[200:201]
	v_pk_fma_f32 v[250:251], v[192:193], v[192:193], v[250:251]
	v_pk_fma_f32 v[250:251], v[194:195], v[194:195], v[250:251]
	v_cvt_pk_f16_f32 v196, v192, v193
	v_cvt_pk_f16_f32 v197, v194, v195
	global_store_dwordx2 v242, v[196:197], s[38:39] offset:96
	s_add_u32 s38, s38, 0x80
	s_addc_u32 s39, s39, 0
	s_waitcnt vmcnt(11)
	s_waitcnt lgkmcnt(0)
	s_barrier
	ds_read_b128 v[144:147], v20 offset:16384
	ds_read_b128 v[148:151], v20 offset:20480
	ds_read_b128 v[152:155], v20 offset:24576
	ds_read_b128 v[156:159], v20 offset:28672
	ds_read_b32 v189, v37 offset:49152
	s_add_u32 m0, s43, 0x0
	s_nop 0
	global_load_lds_dwordx4 v4, s[30:31]
	s_add_u32 m0, s43, 0x4000
	s_nop 0
	global_load_lds_dwordx4 v6, s[32:33]
	s_add_u32 m0, s43, 0x8000
	s_nop 0
	global_load_lds_dwordx4 v8, s[34:35]
	s_add_u32 m0, s43, 0x2000
	s_nop 0
	global_load_lds_dwordx4 v5, s[30:31]
	s_add_u32 m0, s43, 0x6000
	s_nop 0
	global_load_lds_dwordx4 v7, s[32:33]
	s_add_u32 m0, s43, 0xa000
	s_nop 0
	global_load_lds_dwordx4 v9, s[34:35]
	s_add_u32 m0, s44, 0xc000
	s_nop 0
	global_load_lds_dword v10, s[36:37]
	s_add_u32 s30, s30, 0x80000
	s_addc_u32 s31, s31, 0
	s_add_u32 s32, s32, 0x4000
	s_addc_u32 s33, s33, 0
	s_add_u32 s34, s34, 0x80
	s_addc_u32 s35, s35, 0
	s_add_u32 s36, s36, 0x4000
	s_addc_u32 s37, s37, 0
	ds_read_b128 v[160:163], v21 offset:16384
	ds_read_b128 v[164:167], v21 offset:20480
	ds_read_b128 v[168:171], v21 offset:24576
	ds_read_b128 v[172:175], v21 offset:28672
	s_waitcnt lgkmcnt(4)
	v_mfma_f32_16x16x32_f16 v[96:99], v[144:147], v[44:47], 0
	v_mfma_f32_16x16x32_f16 v[100:103], v[148:151], v[44:47], 0
	v_mfma_f32_16x16x32_f16 v[104:107], v[152:155], v[44:47], 0
	v_mfma_f32_16x16x32_f16 v[108:111], v[156:159], v[44:47], 0
	ds_read_b128 v[144:147], v22 offset:16384
	ds_read_b128 v[148:151], v22 offset:20480
	ds_read_b128 v[152:155], v22 offset:24576
	ds_read_b128 v[156:159], v22 offset:28672
	s_waitcnt lgkmcnt(4)
	v_mfma_f32_16x16x32_f16 v[96:99], v[160:163], v[48:51], v[96:99]
	v_mfma_f32_16x16x32_f16 v[100:103], v[164:167], v[48:51], v[100:103]
	v_mfma_f32_16x16x32_f16 v[104:107], v[168:171], v[48:51], v[104:107]
	v_mfma_f32_16x16x32_f16 v[108:111], v[172:175], v[48:51], v[108:111]
	ds_read_b128 v[160:163], v23 offset:16384
	ds_read_b128 v[164:167], v23 offset:20480
	ds_read_b128 v[168:171], v23 offset:24576
	ds_read_b128 v[172:175], v23 offset:28672
	s_waitcnt lgkmcnt(4)
	v_mfma_f32_16x16x32_f16 v[96:99], v[144:147], v[52:55], v[96:99]
	v_mfma_f32_16x16x32_f16 v[100:103], v[148:151], v[52:55], v[100:103]
	v_mfma_f32_16x16x32_f16 v[104:107], v[152:155], v[52:55], v[104:107]
	v_mfma_f32_16x16x32_f16 v[108:111], v[156:159], v[52:55], v[108:111]
	ds_read_b128 v[176:179], v39 offset:49664
	ds_read_b128 v[180:183], v39 offset:49680
	ds_read_b32 v188, v39 offset:49152
	ds_read_b128 v[144:147], v20 offset:0
	ds_read_b128 v[148:151], v20 offset:4096
	ds_read_b128 v[152:155], v20 offset:8192
	ds_read_b128 v[156:159], v20 offset:12288
	s_waitcnt lgkmcnt(7)
	v_mfma_f32_16x16x32_f16 v[96:99], v[160:163], v[56:59], v[96:99]
	v_mfma_f32_16x16x32_f16 v[100:103], v[164:167], v[56:59], v[100:103]
	v_mfma_f32_16x16x32_f16 v[104:107], v[168:171], v[56:59], v[104:107]
	v_mfma_f32_16x16x32_f16 v[108:111], v[172:175], v[56:59], v[108:111]
	v_mul_f32_e32 v189, 0x3fb8aa3b, v189
	s_cmp_lt_u32 s42, 0
	s_cbranch_scc1 .Lmy_s2_kend10
	s_cmp_eq_u32 s42, 0
	s_cbranch_scc1 .Lmy_s2_diag11
	ds_read_b128 v[224:227], v39 offset:49792
	ds_read_b128 v[228:231], v39 offset:49808
	ds_read_b32 v232, v39 offset:49280
	ds_read_b128 v[160:163], v21 offset:0
	ds_read_b128 v[164:167], v21 offset:4096
	ds_read_b128 v[168:171], v21 offset:8192
	ds_read_b128 v[172:175], v21 offset:12288
	s_waitcnt lgkmcnt(7)
	v_fma_f32 v188, v188, s51, v189
	v_exp_f32_e32 v188, v188
	s_nop 0
	v_pk_mul_f32 v[176:177], v[176:177], v[188:189] op_sel_hi:[1,0]
	v_pk_mul_f32 v[178:179], v[178:179], v[188:189] op_sel_hi:[1,0]
	v_pk_mul_f32 v[180:181], v[180:181], v[188:189] op_sel_hi:[1,0]
	v_pk_mul_f32 v[182:183], v[182:183], v[188:189] op_sel_hi:[1,0]
	v_pk_mul_f32 v[176:177], v[60:61], v[176:177]
	v_pk_mul_f32 v[178:179], v[62:63], v[178:179]
	v_pk_mul_f32 v[180:181], v[64:65], v[180:181]
	v_pk_mul_f32 v[182:183], v[66:67], v[182:183]
	v_cvt_pk_f16_f32 v184, v176, v177
	v_cvt_pk_f16_f32 v185, v178, v179
	v_cvt_pk_f16_f32 v186, v180, v181
	v_cvt_pk_f16_f32 v187, v182, v183
	s_nop 1
	v_mfma_f32_16x16x32_f16 v[112:115], v[144:147], v[184:187], 0
	v_mfma_f32_16x16x32_f16 v[116:119], v[148:151], v[184:187], 0
	v_mfma_f32_16x16x32_f16 v[120:123], v[152:155], v[184:187], 0
	v_mfma_f32_16x16x32_f16 v[124:127], v[156:159], v[184:187], 0
	s_branch .Lmy_s2_knext12
.Lmy_s2_diag11:
	ds_read_b64 v[234:235], v28 offset:32768
	ds_read_b64 v[236:237], v29 offset:32768
	ds_read_b64 v[238:239], v30 offset:32768
	ds_read_b64 v[240:241], v31 offset:32768
	s_waitcnt lgkmcnt(4)
	v_fma_f32 v188, v188, s51, v189
	v_exp_f32_e32 v188, v188
	s_nop 0
	v_pk_mul_f32 v[176:177], v[176:177], v[188:189] op_sel_hi:[1,0]
	v_pk_mul_f32 v[178:179], v[178:179], v[188:189] op_sel_hi:[1,0]
	v_pk_mul_f32 v[180:181], v[180:181], v[188:189] op_sel_hi:[1,0]
	v_pk_mul_f32 v[182:183], v[182:183], v[188:189] op_sel_hi:[1,0]
	v_pk_mul_f32 v[176:177], v[60:61], v[176:177]
	v_pk_mul_f32 v[178:179], v[62:63], v[178:179]
	v_pk_mul_f32 v[180:181], v[64:65], v[180:181]
	v_pk_mul_f32 v[182:183], v[66:67], v[182:183]
	v_cndmask_b32_e64 v176, 0, v176, s[52:53]
	v_cndmask_b32_e64 v177, 0, v177, s[54:55]
	v_cndmask_b32_e64 v178, 0, v178, s[56:57]
	v_cndmask_b32_e64 v179, 0, v179, s[58:59]
	v_cndmask_b32_e64 v180, 0, v180, s[60:61]
	v_cndmask_b32_e64 v181, 0, v181, s[62:63]
	v_cndmask_b32_e64 v182, 0, v182, s[64:65]
	v_cndmask_b32_e64 v183, 0, v183, s[66:67]
	v_cvt_pk_f16_f32 v184, v176, v177
	v_cvt_pk_f16_f32 v185, v178, v179
	v_cvt_pk_f16_f32 v186, v180, v181
	v_cvt_pk_f16_f32 v187, v182, v183
	s_nop 1
	v_mfma_f32_16x16x32_f16 v[112:115], v[144:147], v[184:187], 0
	v_mfma_f32_16x16x32_f16 v[116:119], v[148:151], v[184:187], 0
	v_mfma_f32_16x16x32_f16 v[120:123], v[152:155], v[184:187], 0
	v_mfma_f32_16x16x32_f16 v[124:127], v[156:159], v[184:187], 0
	v_mfma_f32_16x16x32_f16 v[128:131], v[144:147], v[92:95], 0
	v_mfma_f32_16x16x32_f16 v[132:135], v[148:151], v[92:95], 0
	v_mfma_f32_16x16x32_f16 v[136:139], v[152:155], v[92:95], 0
	v_mfma_f32_16x16x32_f16 v[140:143], v[156:159], v[92:95], 0
	s_branch .Lmy_s2_kend10
.Lmy_s2_knext12:
	s_cmp_lt_u32 s42, 1
	s_cbranch_scc1 .Lmy_s2_kend10
	s_cmp_eq_u32 s42, 1
	s_cbranch_scc1 .Lmy_s2_diag13
	ds_read_b128 v[176:179], v39 offset:49920
	ds_read_b128 v[180:183], v39 offset:49936
	ds_read_b32 v188, v39 offset:49408
	ds_read_b128 v[144:147], v22 offset:0
	ds_read_b128 v[148:151], v22 offset:4096
	ds_read_b128 v[152:155], v22 offset:8192
	ds_read_b128 v[156:159], v22 offset:12288
	s_waitcnt lgkmcnt(7)
	v_fma_f32 v232, v232, s51, v189
	v_exp_f32_e32 v232, v232
	s_nop 0
	v_pk_mul_f32 v[224:225], v[224:225], v[232:233] op_sel_hi:[1,0]
	v_pk_mul_f32 v[226:227], v[226:227], v[232:233] op_sel_hi:[1,0]
	v_pk_mul_f32 v[228:229], v[228:229], v[232:233] op_sel_hi:[1,0]
	v_pk_mul_f32 v[230:231], v[230:231], v[232:233] op_sel_hi:[1,0]
	v_pk_mul_f32 v[224:225], v[68:69], v[224:225]
	v_pk_mul_f32 v[226:227], v[70:71], v[226:227]
	v_pk_mul_f32 v[228:229], v[72:73], v[228:229]
	v_pk_mul_f32 v[230:231], v[74:75], v[230:231]
	v_cvt_pk_f16_f32 v184, v224, v225
	v_cvt_pk_f16_f32 v185, v226, v227
	v_cvt_pk_f16_f32 v186, v228, v229
	v_cvt_pk_f16_f32 v187, v230, v231
	s_nop 1
	v_mfma_f32_16x16x32_f16 v[112:115], v[160:163], v[184:187], v[112:115]
	v_mfma_f32_16x16x32_f16 v[116:119], v[164:167], v[184:187], v[116:119]
	v_mfma_f32_16x16x32_f16 v[120:123], v[168:171], v[184:187], v[120:123]
	v_mfma_f32_16x16x32_f16 v[124:127], v[172:175], v[184:187], v[124:127]
	s_branch .Lmy_s2_knext14
.Lmy_s2_diag13:
	ds_read_b64 v[234:235], v28 offset:32768
	ds_read_b64 v[236:237], v29 offset:32768
	ds_read_b64 v[238:239], v30 offset:32768
	ds_read_b64 v[240:241], v31 offset:32768
	s_waitcnt lgkmcnt(4)
	v_fma_f32 v232, v232, s51, v189
	v_exp_f32_e32 v232, v232
	s_nop 0
	v_pk_mul_f32 v[224:225], v[224:225], v[232:233] op_sel_hi:[1,0]
	v_pk_mul_f32 v[226:227], v[226:227], v[232:233] op_sel_hi:[1,0]
	v_pk_mul_f32 v[228:229], v[228:229], v[232:233] op_sel_hi:[1,0]
	v_pk_mul_f32 v[230:231], v[230:231], v[232:233] op_sel_hi:[1,0]
	v_pk_mul_f32 v[224:225], v[68:69], v[224:225]
	v_pk_mul_f32 v[226:227], v[70:71], v[226:227]
	v_pk_mul_f32 v[228:229], v[72:73], v[228:229]
	v_pk_mul_f32 v[230:231], v[74:75], v[230:231]
	v_cndmask_b32_e64 v224, 0, v224, s[52:53]
	v_cndmask_b32_e64 v225, 0, v225, s[54:55]
	v_cndmask_b32_e64 v226, 0, v226, s[56:57]
	v_cndmask_b32_e64 v227, 0, v227, s[58:59]
	v_cndmask_b32_e64 v228, 0, v228, s[60:61]
	v_cndmask_b32_e64 v229, 0, v229, s[62:63]
	v_cndmask_b32_e64 v230, 0, v230, s[64:65]
	v_cndmask_b32_e64 v231, 0, v231, s[66:67]
	v_cvt_pk_f16_f32 v184, v224, v225
	v_cvt_pk_f16_f32 v185, v226, v227
	v_cvt_pk_f16_f32 v186, v228, v229
	v_cvt_pk_f16_f32 v187, v230, v231
	s_nop 1
	v_mfma_f32_16x16x32_f16 v[112:115], v[160:163], v[184:187], v[112:115]
	v_mfma_f32_16x16x32_f16 v[116:119], v[164:167], v[184:187], v[116:119]
	v_mfma_f32_16x16x32_f16 v[120:123], v[168:171], v[184:187], v[120:123]
	v_mfma_f32_16x16x32_f16 v[124:127], v[172:175], v[184:187], v[124:127]
	v_mfma_f32_16x16x32_f16 v[128:131], v[160:163], v[92:95], 0
	v_mfma_f32_16x16x32_f16 v[132:135], v[164:167], v[92:95], 0
	v_mfma_f32_16x16x32_f16 v[136:139], v[168:171], v[92:95], 0
	v_mfma_f32_16x16x32_f16 v[140:143], v[172:175], v[92:95], 0
	s_branch .Lmy_s2_kend10
.Lmy_s2_knext14:
	s_cmp_lt_u32 s42, 2
	s_cbranch_scc1 .Lmy_s2_kend10
	s_cmp_eq_u32 s42, 2
	s_cbranch_scc1 .Lmy_s2_diag15
	ds_read_b128 v[224:227], v39 offset:50048
	ds_read_b128 v[228:231], v39 offset:50064
	ds_read_b32 v232, v39 offset:49536
	ds_read_b128 v[160:163], v23 offset:0
	ds_read_b128 v[164:167], v23 offset:4096
	ds_read_b128 v[168:171], v23 offset:8192
	ds_read_b128 v[172:175], v23 offset:12288
	s_waitcnt lgkmcnt(7)
	v_fma_f32 v188, v188, s51, v189
	v_exp_f32_e32 v188, v188
	s_nop 0
	v_pk_mul_f32 v[176:177], v[176:177], v[188:189] op_sel_hi:[1,0]
	v_pk_mul_f32 v[178:179], v[178:179], v[188:189] op_sel_hi:[1,0]
	v_pk_mul_f32 v[180:181], v[180:181], v[188:189] op_sel_hi:[1,0]
	v_pk_mul_f32 v[182:183], v[182:183], v[188:189] op_sel_hi:[1,0]
	v_pk_mul_f32 v[176:177], v[76:77], v[176:177]
	v_pk_mul_f32 v[178:179], v[78:79], v[178:179]
	v_pk_mul_f32 v[180:181], v[80:81], v[180:181]
	v_pk_mul_f32 v[182:183], v[82:83], v[182:183]
	v_cvt_pk_f16_f32 v184, v176, v177
	v_cvt_pk_f16_f32 v185, v178, v179
	v_cvt_pk_f16_f32 v186, v180, v181
	v_cvt_pk_f16_f32 v187, v182, v183
	s_nop 1
	v_mfma_f32_16x16x32_f16 v[112:115], v[144:147], v[184:187], v[112:115]
	v_mfma_f32_16x16x32_f16 v[116:119], v[148:151], v[184:187], v[116:119]
	v_mfma_f32_16x16x32_f16 v[120:123], v[152:155], v[184:187], v[120:123]
	v_mfma_f32_16x16x32_f16 v[124:127], v[156:159], v[184:187], v[124:127]
	s_branch .Lmy_s2_knext16
.Lmy_s2_diag15:
	ds_read_b64 v[234:235], v28 offset:32768
	ds_read_b64 v[236:237], v29 offset:32768
	ds_read_b64 v[238:239], v30 offset:32768
	ds_read_b64 v[240:241], v31 offset:32768
	s_waitcnt lgkmcnt(4)
	v_fma_f32 v188, v188, s51, v189
	v_exp_f32_e32 v188, v188
	s_nop 0
	v_pk_mul_f32 v[176:177], v[176:177], v[188:189] op_sel_hi:[1,0]
	v_pk_mul_f32 v[178:179], v[178:179], v[188:189] op_sel_hi:[1,0]
	v_pk_mul_f32 v[180:181], v[180:181], v[188:189] op_sel_hi:[1,0]
	v_pk_mul_f32 v[182:183], v[182:183], v[188:189] op_sel_hi:[1,0]
	v_pk_mul_f32 v[176:177], v[76:77], v[176:177]
	v_pk_mul_f32 v[178:179], v[78:79], v[178:179]
	v_pk_mul_f32 v[180:181], v[80:81], v[180:181]
	v_pk_mul_f32 v[182:183], v[82:83], v[182:183]
	v_cndmask_b32_e64 v176, 0, v176, s[52:53]
	v_cndmask_b32_e64 v177, 0, v177, s[54:55]
	v_cndmask_b32_e64 v178, 0, v178, s[56:57]
	v_cndmask_b32_e64 v179, 0, v179, s[58:59]
	v_cndmask_b32_e64 v180, 0, v180, s[60:61]
	v_cndmask_b32_e64 v181, 0, v181, s[62:63]
	v_cndmask_b32_e64 v182, 0, v182, s[64:65]
	v_cndmask_b32_e64 v183, 0, v183, s[66:67]
	v_cvt_pk_f16_f32 v184, v176, v177
	v_cvt_pk_f16_f32 v185, v178, v179
	v_cvt_pk_f16_f32 v186, v180, v181
	v_cvt_pk_f16_f32 v187, v182, v183
	s_nop 1
	v_mfma_f32_16x16x32_f16 v[112:115], v[144:147], v[184:187], v[112:115]
	v_mfma_f32_16x16x32_f16 v[116:119], v[148:151], v[184:187], v[116:119]
	v_mfma_f32_16x16x32_f16 v[120:123], v[152:155], v[184:187], v[120:123]
	v_mfma_f32_16x16x32_f16 v[124:127], v[156:159], v[184:187], v[124:127]
	v_mfma_f32_16x16x32_f16 v[128:131], v[144:147], v[92:95], 0
	v_mfma_f32_16x16x32_f16 v[132:135], v[148:151], v[92:95], 0
	v_mfma_f32_16x16x32_f16 v[136:139], v[152:155], v[92:95], 0
	v_mfma_f32_16x16x32_f16 v[140:143], v[156:159], v[92:95], 0
	s_branch .Lmy_s2_kend10

.Lmy_s2_diag17:
	ds_read_b64 v[234:235], v28 offset:32768
	ds_read_b64 v[236:237], v29 offset:32768
	ds_read_b64 v[238:239], v30 offset:32768
	ds_read_b64 v[240:241], v31 offset:32768
	s_waitcnt lgkmcnt(4)
	v_fma_f32 v232, v232, s51, v189
	v_exp_f32_e32 v232, v232
	s_nop 0
	v_pk_mul_f32 v[224:225], v[224:225], v[232:233] op_sel_hi:[1,0]
	v_pk_mul_f32 v[226:227], v[226:227], v[232:233] op_sel_hi:[1,0]
	v_pk_mul_f32 v[228:229], v[228:229], v[232:233] op_sel_hi:[1,0]
	v_pk_mul_f32 v[230:231], v[230:231], v[232:233] op_sel_hi:[1,0]
	v_pk_mul_f32 v[224:225], v[84:85], v[224:225]
	v_pk_mul_f32 v[226:227], v[86:87], v[226:227]
	v_pk_mul_f32 v[228:229], v[88:89], v[228:229]
	v_pk_mul_f32 v[230:231], v[90:91], v[230:231]
	v_cndmask_b32_e64 v224, 0, v224, s[52:53]
	v_cndmask_b32_e64 v225, 0, v225, s[54:55]
	v_cndmask_b32_e64 v226, 0, v226, s[56:57]
	v_cndmask_b32_e64 v227, 0, v227, s[58:59]
	v_cndmask_b32_e64 v228, 0, v228, s[60:61]
	v_cndmask_b32_e64 v229, 0, v229, s[62:63]
	v_cndmask_b32_e64 v230, 0, v230, s[64:65]
	v_cndmask_b32_e64 v231, 0, v231, s[66:67]
	v_cvt_pk_f16_f32 v184, v224, v225
	v_cvt_pk_f16_f32 v185, v226, v227
	v_cvt_pk_f16_f32 v186, v228, v229
	v_cvt_pk_f16_f32 v187, v230, v231
	s_nop 1
	v_mfma_f32_16x16x32_f16 v[112:115], v[160:163], v[184:187], v[112:115]
	v_mfma_f32_16x16x32_f16 v[116:119], v[164:167], v[184:187], v[116:119]
	v_mfma_f32_16x16x32_f16 v[120:123], v[168:171], v[184:187], v[120:123]
	v_mfma_f32_16x16x32_f16 v[124:127], v[172:175], v[184:187], v[124:127]
	v_mfma_f32_16x16x32_f16 v[128:131], v[160:163], v[92:95], 0
	v_mfma_f32_16x16x32_f16 v[132:135], v[164:167], v[92:95], 0
	v_mfma_f32_16x16x32_f16 v[136:139], v[168:171], v[92:95], 0
	v_mfma_f32_16x16x32_f16 v[140:143], v[172:175], v[92:95], 0
	s_branch .Lmy_s2_kend10
.Lmy_s2_knext18:
.Lmy_s2_kend10:
	v_readlane_b32 s46, v11, 1
	v_readlane_b32 s47, v12, 1
	v_exp_f32_e32 v190, v189
	s_waitcnt lgkmcnt(0)
	s_nop 7
	v_cvt_f32_f16_e32 v198, v234
	v_cvt_f32_f16_sdwa v199, v234 dst_sel:DWORD dst_unused:UNUSED_PAD src0_sel:WORD_1
	v_cvt_f32_f16_e32 v200, v235
	v_cvt_f32_f16_sdwa v201, v235 dst_sel:DWORD dst_unused:UNUSED_PAD src0_sel:WORD_1
	v_pk_fma_f32 v[192:193], v[190:191], v[96:97], v[112:113] op_sel_hi:[0,1,1]
	v_pk_fma_f32 v[194:195], v[190:191], v[98:99], v[114:115] op_sel_hi:[0,1,1]
	v_pk_mul_f32 v[192:193], v[192:193], s[46:47] op_sel:[0,1] op_sel_hi:[1,1]
	v_pk_mul_f32 v[194:195], v[194:195], s[46:47] op_sel:[0,1] op_sel_hi:[1,1]
	v_pk_fma_f32 v[192:193], s[46:47], v[128:129], v[192:193] op_sel_hi:[0,1,1]
	v_pk_fma_f32 v[194:195], s[46:47], v[130:131], v[194:195] op_sel_hi:[0,1,1]
	v_pk_mul_f32 v[192:193], v[192:193], v[198:199]
	v_pk_mul_f32 v[194:195], v[194:195], v[200:201]
	v_pk_fma_f32 v[250:251], v[192:193], v[192:193], v[250:251]
	v_pk_fma_f32 v[250:251], v[194:195], v[194:195], v[250:251]
	v_cvt_pk_f16_f32 v196, v192, v193
	v_cvt_pk_f16_f32 v197, v194, v195
	global_store_dwordx2 v242, v[196:197], s[38:39]
	v_cvt_f32_f16_e32 v198, v236
	v_cvt_f32_f16_sdwa v199, v236 dst_sel:DWORD dst_unused:UNUSED_PAD src0_sel:WORD_1
	v_cvt_f32_f16_e32 v200, v237
	v_cvt_f32_f16_sdwa v201, v237 dst_sel:DWORD dst_unused:UNUSED_PAD src0_sel:WORD_1
	v_pk_fma_f32 v[192:193], v[190:191], v[100:101], v[116:117] op_sel_hi:[0,1,1]
	v_pk_fma_f32 v[194:195], v[190:191], v[102:103], v[118:119] op_sel_hi:[0,1,1]
	v_pk_mul_f32 v[192:193], v[192:193], s[46:47] op_sel:[0,1] op_sel_hi:[1,1]
	v_pk_mul_f32 v[194:195], v[194:195], s[46:47] op_sel:[0,1] op_sel_hi:[1,1]
	v_pk_fma_f32 v[192:193], s[46:47], v[132:133], v[192:193] op_sel_hi:[0,1,1]
	v_pk_fma_f32 v[194:195], s[46:47], v[134:135], v[194:195] op_sel_hi:[0,1,1]
	v_pk_mul_f32 v[192:193], v[192:193], v[198:199]
	v_pk_mul_f32 v[194:195], v[194:195], v[200:201]
	v_pk_fma_f32 v[250:251], v[192:193], v[192:193], v[250:251]
	v_pk_fma_f32 v[250:251], v[194:195], v[194:195], v[250:251]
	v_cvt_pk_f16_f32 v196, v192, v193
	v_cvt_pk_f16_f32 v197, v194, v195
	global_store_dwordx2 v242, v[196:197], s[38:39] offset:32
	v_cvt_f32_f16_e32 v198, v238
	v_cvt_f32_f16_sdwa v199, v238 dst_sel:DWORD dst_unused:UNUSED_PAD src0_sel:WORD_1
	v_cvt_f32_f16_e32 v200, v239
	v_cvt_f32_f16_sdwa v201, v239 dst_sel:DWORD dst_unused:UNUSED_PAD src0_sel:WORD_1
	v_pk_fma_f32 v[192:193], v[190:191], v[104:105], v[120:121] op_sel_hi:[0,1,1]
	v_pk_fma_f32 v[194:195], v[190:191], v[106:107], v[122:123] op_sel_hi:[0,1,1]
	v_pk_mul_f32 v[192:193], v[192:193], s[46:47] op_sel:[0,1] op_sel_hi:[1,1]
	v_pk_mul_f32 v[194:195], v[194:195], s[46:47] op_sel:[0,1] op_sel_hi:[1,1]
	v_pk_fma_f32 v[192:193], s[46:47], v[136:137], v[192:193] op_sel_hi:[0,1,1]
	v_pk_fma_f32 v[194:195], s[46:47], v[138:139], v[194:195] op_sel_hi:[0,1,1]
	v_pk_mul_f32 v[192:193], v[192:193], v[198:199]
	v_pk_mul_f32 v[194:195], v[194:195], v[200:201]
	v_pk_fma_f32 v[250:251], v[192:193], v[192:193], v[250:251]
	v_pk_fma_f32 v[250:251], v[194:195], v[194:195], v[250:251]
	v_cvt_pk_f16_f32 v196, v192, v193
	v_cvt_pk_f16_f32 v197, v194, v195
	global_store_dwordx2 v242, v[196:197], s[38:39] offset:64
	v_cvt_f32_f16_e32 v198, v240
	v_cvt_f32_f16_sdwa v199, v240 dst_sel:DWORD dst_unused:UNUSED_PAD src0_sel:WORD_1
	v_cvt_f32_f16_e32 v200, v241
	v_cvt_f32_f16_sdwa v201, v241 dst_sel:DWORD dst_unused:UNUSED_PAD src0_sel:WORD_1
	v_pk_fma_f32 v[192:193], v[190:191], v[108:109], v[124:125] op_sel_hi:[0,1,1]
	v_pk_fma_f32 v[194:195], v[190:191], v[110:111], v[126:127] op_sel_hi:[0,1,1]
	v_pk_mul_f32 v[192:193], v[192:193], s[46:47] op_sel:[0,1] op_sel_hi:[1,1]
	v_pk_mul_f32 v[194:195], v[194:195], s[46:47] op_sel:[0,1] op_sel_hi:[1,1]
	v_pk_fma_f32 v[192:193], s[46:47], v[140:141], v[192:193] op_sel_hi:[0,1,1]
	v_pk_fma_f32 v[194:195], s[46:47], v[142:143], v[194:195] op_sel_hi:[0,1,1]
	v_pk_mul_f32 v[192:193], v[192:193], v[198:199]
	v_pk_mul_f32 v[194:195], v[194:195], v[200:201]
	v_pk_fma_f32 v[250:251], v[192:193], v[192:193], v[250:251]
	v_pk_fma_f32 v[250:251], v[194:195], v[194:195], v[250:251]
	v_cvt_pk_f16_f32 v196, v192, v193
	v_cvt_pk_f16_f32 v197, v194, v195
	global_store_dwordx2 v242, v[196:197], s[38:39] offset:96
	s_add_u32 s38, s38, 0x80
	s_addc_u32 s39, s39, 0
	s_waitcnt vmcnt(15)
	s_waitcnt lgkmcnt(0)
	s_barrier
	ds_read_b128 v[144:147], v212 offset:16384
	ds_read_b128 v[148:151], v212 offset:20480
	ds_read_b128 v[152:155], v212 offset:24576
	ds_read_b128 v[156:159], v212 offset:28672
	ds_read_b32 v189, v220 offset:49152
	s_add_u32 m0, s43, 0xc800
	s_nop 0
	global_load_lds_dwordx4 v4, s[30:31]
	s_add_u32 m0, s43, 0x10800
	s_nop 0
	global_load_lds_dwordx4 v6, s[32:33]
	s_add_u32 m0, s43, 0x14800
	s_nop 0
	global_load_lds_dwordx4 v8, s[34:35]
	s_add_u32 m0, s43, 0xe800
	s_nop 0
	global_load_lds_dwordx4 v5, s[30:31]
	s_add_u32 m0, s43, 0x12800
	s_nop 0
	global_load_lds_dwordx4 v7, s[32:33]
	s_add_u32 m0, s43, 0x16800
	s_nop 0
	global_load_lds_dwordx4 v9, s[34:35]
	s_add_u32 m0, s44, 0x18800
	s_nop 0
	global_load_lds_dword v10, s[36:37]
	s_add_u32 s30, s30, 0x80000
	s_addc_u32 s31, s31, 0
	s_add_u32 s32, s32, 0x4000
	s_addc_u32 s33, s33, 0
	s_add_u32 s34, s34, 0x80
	s_addc_u32 s35, s35, 0
	s_add_u32 s36, s36, 0x4000
	s_addc_u32 s37, s37, 0
	ds_read_b128 v[160:163], v213 offset:16384
	ds_read_b128 v[164:167], v213 offset:20480
	ds_read_b128 v[168:171], v213 offset:24576
	ds_read_b128 v[172:175], v213 offset:28672
	s_waitcnt lgkmcnt(4)
	v_mfma_f32_16x16x32_f16 v[96:99], v[144:147], v[44:47], 0
	v_mfma_f32_16x16x32_f16 v[100:103], v[148:151], v[44:47], 0
	v_mfma_f32_16x16x32_f16 v[104:107], v[152:155], v[44:47], 0
	v_mfma_f32_16x16x32_f16 v[108:111], v[156:159], v[44:47], 0
	ds_read_b128 v[144:147], v214 offset:16384
	ds_read_b128 v[148:151], v214 offset:20480
	ds_read_b128 v[152:155], v214 offset:24576
	ds_read_b128 v[156:159], v214 offset:28672
	s_waitcnt lgkmcnt(4)
	v_mfma_f32_16x16x32_f16 v[96:99], v[160:163], v[48:51], v[96:99]
	v_mfma_f32_16x16x32_f16 v[100:103], v[164:167], v[48:51], v[100:103]
	v_mfma_f32_16x16x32_f16 v[104:107], v[168:171], v[48:51], v[104:107]
	v_mfma_f32_16x16x32_f16 v[108:111], v[172:175], v[48:51], v[108:111]
	ds_read_b128 v[160:163], v215 offset:16384
	ds_read_b128 v[164:167], v215 offset:20480
	ds_read_b128 v[168:171], v215 offset:24576
	ds_read_b128 v[172:175], v215 offset:28672
	s_waitcnt lgkmcnt(4)
	v_mfma_f32_16x16x32_f16 v[96:99], v[144:147], v[52:55], v[96:99]
	v_mfma_f32_16x16x32_f16 v[100:103], v[148:151], v[52:55], v[100:103]
	v_mfma_f32_16x16x32_f16 v[104:107], v[152:155], v[52:55], v[104:107]
	v_mfma_f32_16x16x32_f16 v[108:111], v[156:159], v[52:55], v[108:111]
	ds_read_b128 v[176:179], v221 offset:49664
	ds_read_b128 v[180:183], v221 offset:49680
	ds_read_b32 v188, v221 offset:49152
	ds_read_b128 v[144:147], v212 offset:0
	ds_read_b128 v[148:151], v212 offset:4096
	ds_read_b128 v[152:155], v212 offset:8192
	ds_read_b128 v[156:159], v212 offset:12288
	s_waitcnt lgkmcnt(7)
	v_mfma_f32_16x16x32_f16 v[96:99], v[160:163], v[56:59], v[96:99]
	v_mfma_f32_16x16x32_f16 v[100:103], v[164:167], v[56:59], v[100:103]
	v_mfma_f32_16x16x32_f16 v[104:107], v[168:171], v[56:59], v[104:107]
	v_mfma_f32_16x16x32_f16 v[108:111], v[172:175], v[56:59], v[108:111]
	v_mul_f32_e32 v189, 0x3fb8aa3b, v189
	s_cmp_lt_u32 s42, 0
	s_cbranch_scc1 .Lmy_s2_kend19
	s_cmp_eq_u32 s42, 0
	s_cbranch_scc1 .Lmy_s2_diag20
	ds_read_b128 v[224:227], v221 offset:49792
	ds_read_b128 v[228:231], v221 offset:49808
	ds_read_b32 v232, v221 offset:49280
	ds_read_b128 v[160:163], v213 offset:0
	ds_read_b128 v[164:167], v213 offset:4096
	ds_read_b128 v[168:171], v213 offset:8192
	ds_read_b128 v[172:175], v213 offset:12288
	s_waitcnt lgkmcnt(7)
	v_fma_f32 v188, v188, s51, v189
	v_exp_f32_e32 v188, v188
	s_nop 0
	v_pk_mul_f32 v[176:177], v[176:177], v[188:189] op_sel_hi:[1,0]
	v_pk_mul_f32 v[178:179], v[178:179], v[188:189] op_sel_hi:[1,0]
	v_pk_mul_f32 v[180:181], v[180:181], v[188:189] op_sel_hi:[1,0]
	v_pk_mul_f32 v[182:183], v[182:183], v[188:189] op_sel_hi:[1,0]
	v_pk_mul_f32 v[176:177], v[60:61], v[176:177]
	v_pk_mul_f32 v[178:179], v[62:63], v[178:179]
	v_pk_mul_f32 v[180:181], v[64:65], v[180:181]
	v_pk_mul_f32 v[182:183], v[66:67], v[182:183]
	v_cvt_pk_f16_f32 v184, v176, v177
	v_cvt_pk_f16_f32 v185, v178, v179
	v_cvt_pk_f16_f32 v186, v180, v181
	v_cvt_pk_f16_f32 v187, v182, v183
	s_nop 1
	v_mfma_f32_16x16x32_f16 v[112:115], v[144:147], v[184:187], 0
	v_mfma_f32_16x16x32_f16 v[116:119], v[148:151], v[184:187], 0
	v_mfma_f32_16x16x32_f16 v[120:123], v[152:155], v[184:187], 0
	v_mfma_f32_16x16x32_f16 v[124:127], v[156:159], v[184:187], 0
	s_branch .Lmy_s2_knext21
.Lmy_s2_diag20:
	ds_read_b64 v[234:235], v216 offset:32768
	ds_read_b64 v[236:237], v217 offset:32768
	ds_read_b64 v[238:239], v218 offset:32768
	ds_read_b64 v[240:241], v219 offset:32768
	s_waitcnt lgkmcnt(4)
	v_fma_f32 v188, v188, s51, v189
	v_exp_f32_e32 v188, v188
	s_nop 0
	v_pk_mul_f32 v[176:177], v[176:177], v[188:189] op_sel_hi:[1,0]
	v_pk_mul_f32 v[178:179], v[178:179], v[188:189] op_sel_hi:[1,0]
	v_pk_mul_f32 v[180:181], v[180:181], v[188:189] op_sel_hi:[1,0]
	v_pk_mul_f32 v[182:183], v[182:183], v[188:189] op_sel_hi:[1,0]
	v_pk_mul_f32 v[176:177], v[60:61], v[176:177]
	v_pk_mul_f32 v[178:179], v[62:63], v[178:179]
	v_pk_mul_f32 v[180:181], v[64:65], v[180:181]
	v_pk_mul_f32 v[182:183], v[66:67], v[182:183]
	v_cndmask_b32_e64 v176, 0, v176, s[52:53]
	v_cndmask_b32_e64 v177, 0, v177, s[54:55]
	v_cndmask_b32_e64 v178, 0, v178, s[56:57]
	v_cndmask_b32_e64 v179, 0, v179, s[58:59]
	v_cndmask_b32_e64 v180, 0, v180, s[60:61]
	v_cndmask_b32_e64 v181, 0, v181, s[62:63]
	v_cndmask_b32_e64 v182, 0, v182, s[64:65]
	v_cndmask_b32_e64 v183, 0, v183, s[66:67]
	v_cvt_pk_f16_f32 v184, v176, v177
	v_cvt_pk_f16_f32 v185, v178, v179
	v_cvt_pk_f16_f32 v186, v180, v181
	v_cvt_pk_f16_f32 v187, v182, v183
	s_nop 1
	v_mfma_f32_16x16x32_f16 v[112:115], v[144:147], v[184:187], 0
	v_mfma_f32_16x16x32_f16 v[116:119], v[148:151], v[184:187], 0
	v_mfma_f32_16x16x32_f16 v[120:123], v[152:155], v[184:187], 0
	v_mfma_f32_16x16x32_f16 v[124:127], v[156:159], v[184:187], 0
	v_mfma_f32_16x16x32_f16 v[128:131], v[144:147], v[92:95], 0
	v_mfma_f32_16x16x32_f16 v[132:135], v[148:151], v[92:95], 0
	v_mfma_f32_16x16x32_f16 v[136:139], v[152:155], v[92:95], 0
	v_mfma_f32_16x16x32_f16 v[140:143], v[156:159], v[92:95], 0
	s_branch .Lmy_s2_kend19
.Lmy_s2_knext21:
	s_cmp_lt_u32 s42, 1
	s_cbranch_scc1 .Lmy_s2_kend19
	s_cmp_eq_u32 s42, 1
	s_cbranch_scc1 .Lmy_s2_diag22
	ds_read_b128 v[176:179], v221 offset:49920
	ds_read_b128 v[180:183], v221 offset:49936
	ds_read_b32 v188, v221 offset:49408
	ds_read_b128 v[144:147], v214 offset:0
	ds_read_b128 v[148:151], v214 offset:4096
	ds_read_b128 v[152:155], v214 offset:8192
	ds_read_b128 v[156:159], v214 offset:12288
	s_waitcnt lgkmcnt(7)
	v_fma_f32 v232, v232, s51, v189
	v_exp_f32_e32 v232, v232
	s_nop 0
	v_pk_mul_f32 v[224:225], v[224:225], v[232:233] op_sel_hi:[1,0]
	v_pk_mul_f32 v[226:227], v[226:227], v[232:233] op_sel_hi:[1,0]
	v_pk_mul_f32 v[228:229], v[228:229], v[232:233] op_sel_hi:[1,0]
	v_pk_mul_f32 v[230:231], v[230:231], v[232:233] op_sel_hi:[1,0]
	v_pk_mul_f32 v[224:225], v[68:69], v[224:225]
	v_pk_mul_f32 v[226:227], v[70:71], v[226:227]
	v_pk_mul_f32 v[228:229], v[72:73], v[228:229]
	v_pk_mul_f32 v[230:231], v[74:75], v[230:231]
	v_cvt_pk_f16_f32 v184, v224, v225
	v_cvt_pk_f16_f32 v185, v226, v227
	v_cvt_pk_f16_f32 v186, v228, v229
	v_cvt_pk_f16_f32 v187, v230, v231
	s_nop 1
	v_mfma_f32_16x16x32_f16 v[112:115], v[160:163], v[184:187], v[112:115]
	v_mfma_f32_16x16x32_f16 v[116:119], v[164:167], v[184:187], v[116:119]
	v_mfma_f32_16x16x32_f16 v[120:123], v[168:171], v[184:187], v[120:123]
	v_mfma_f32_16x16x32_f16 v[124:127], v[172:175], v[184:187], v[124:127]
	s_branch .Lmy_s2_knext23
.Lmy_s2_diag22:
	ds_read_b64 v[234:235], v216 offset:32768
	ds_read_b64 v[236:237], v217 offset:32768
	ds_read_b64 v[238:239], v218 offset:32768
	ds_read_b64 v[240:241], v219 offset:32768
	s_waitcnt lgkmcnt(4)
	v_fma_f32 v232, v232, s51, v189
	v_exp_f32_e32 v232, v232
	s_nop 0
	v_pk_mul_f32 v[224:225], v[224:225], v[232:233] op_sel_hi:[1,0]
	v_pk_mul_f32 v[226:227], v[226:227], v[232:233] op_sel_hi:[1,0]
	v_pk_mul_f32 v[228:229], v[228:229], v[232:233] op_sel_hi:[1,0]
	v_pk_mul_f32 v[230:231], v[230:231], v[232:233] op_sel_hi:[1,0]
	v_pk_mul_f32 v[224:225], v[68:69], v[224:225]
	v_pk_mul_f32 v[226:227], v[70:71], v[226:227]
	v_pk_mul_f32 v[228:229], v[72:73], v[228:229]
	v_pk_mul_f32 v[230:231], v[74:75], v[230:231]
	v_cndmask_b32_e64 v224, 0, v224, s[52:53]
	v_cndmask_b32_e64 v225, 0, v225, s[54:55]
	v_cndmask_b32_e64 v226, 0, v226, s[56:57]
	v_cndmask_b32_e64 v227, 0, v227, s[58:59]
	v_cndmask_b32_e64 v228, 0, v228, s[60:61]
	v_cndmask_b32_e64 v229, 0, v229, s[62:63]
	v_cndmask_b32_e64 v230, 0, v230, s[64:65]
	v_cndmask_b32_e64 v231, 0, v231, s[66:67]
	v_cvt_pk_f16_f32 v184, v224, v225
	v_cvt_pk_f16_f32 v185, v226, v227
	v_cvt_pk_f16_f32 v186, v228, v229
	v_cvt_pk_f16_f32 v187, v230, v231
	s_nop 1
	v_mfma_f32_16x16x32_f16 v[112:115], v[160:163], v[184:187], v[112:115]
	v_mfma_f32_16x16x32_f16 v[116:119], v[164:167], v[184:187], v[116:119]
	v_mfma_f32_16x16x32_f16 v[120:123], v[168:171], v[184:187], v[120:123]
	v_mfma_f32_16x16x32_f16 v[124:127], v[172:175], v[184:187], v[124:127]
	v_mfma_f32_16x16x32_f16 v[128:131], v[160:163], v[92:95], 0
	v_mfma_f32_16x16x32_f16 v[132:135], v[164:167], v[92:95], 0
	v_mfma_f32_16x16x32_f16 v[136:139], v[168:171], v[92:95], 0
	v_mfma_f32_16x16x32_f16 v[140:143], v[172:175], v[92:95], 0
	s_branch .Lmy_s2_kend19
.Lmy_s2_knext23:
	s_cmp_lt_u32 s42, 2
	s_cbranch_scc1 .Lmy_s2_kend19
	s_cmp_eq_u32 s42, 2
	s_cbranch_scc1 .Lmy_s2_diag24
	ds_read_b128 v[224:227], v221 offset:50048
	ds_read_b128 v[228:231], v221 offset:50064
	ds_read_b32 v232, v221 offset:49536
	ds_read_b128 v[160:163], v215 offset:0
	ds_read_b128 v[164:167], v215 offset:4096
	ds_read_b128 v[168:171], v215 offset:8192
	ds_read_b128 v[172:175], v215 offset:12288
	s_waitcnt lgkmcnt(7)
	v_fma_f32 v188, v188, s51, v189
	v_exp_f32_e32 v188, v188
	s_nop 0
	v_pk_mul_f32 v[176:177], v[176:177], v[188:189] op_sel_hi:[1,0]
	v_pk_mul_f32 v[178:179], v[178:179], v[188:189] op_sel_hi:[1,0]
	v_pk_mul_f32 v[180:181], v[180:181], v[188:189] op_sel_hi:[1,0]
	v_pk_mul_f32 v[182:183], v[182:183], v[188:189] op_sel_hi:[1,0]
	v_pk_mul_f32 v[176:177], v[76:77], v[176:177]
	v_pk_mul_f32 v[178:179], v[78:79], v[178:179]
	v_pk_mul_f32 v[180:181], v[80:81], v[180:181]
	v_pk_mul_f32 v[182:183], v[82:83], v[182:183]
	v_cvt_pk_f16_f32 v184, v176, v177
	v_cvt_pk_f16_f32 v185, v178, v179
	v_cvt_pk_f16_f32 v186, v180, v181
	v_cvt_pk_f16_f32 v187, v182, v183
	s_nop 1
	v_mfma_f32_16x16x32_f16 v[112:115], v[144:147], v[184:187], v[112:115]
	v_mfma_f32_16x16x32_f16 v[116:119], v[148:151], v[184:187], v[116:119]
	v_mfma_f32_16x16x32_f16 v[120:123], v[152:155], v[184:187], v[120:123]
	v_mfma_f32_16x16x32_f16 v[124:127], v[156:159], v[184:187], v[124:127]
	s_branch .Lmy_s2_knext25
.Lmy_s2_diag24:
	ds_read_b64 v[234:235], v216 offset:32768
	ds_read_b64 v[236:237], v217 offset:32768
	ds_read_b64 v[238:239], v218 offset:32768
	ds_read_b64 v[240:241], v219 offset:32768
	s_waitcnt lgkmcnt(4)
	v_fma_f32 v188, v188, s51, v189
	v_exp_f32_e32 v188, v188
	s_nop 0
	v_pk_mul_f32 v[176:177], v[176:177], v[188:189] op_sel_hi:[1,0]
	v_pk_mul_f32 v[178:179], v[178:179], v[188:189] op_sel_hi:[1,0]
	v_pk_mul_f32 v[180:181], v[180:181], v[188:189] op_sel_hi:[1,0]
	v_pk_mul_f32 v[182:183], v[182:183], v[188:189] op_sel_hi:[1,0]
	v_pk_mul_f32 v[176:177], v[76:77], v[176:177]
	v_pk_mul_f32 v[178:179], v[78:79], v[178:179]
	v_pk_mul_f32 v[180:181], v[80:81], v[180:181]
	v_pk_mul_f32 v[182:183], v[82:83], v[182:183]
	v_cndmask_b32_e64 v176, 0, v176, s[52:53]
	v_cndmask_b32_e64 v177, 0, v177, s[54:55]
	v_cndmask_b32_e64 v178, 0, v178, s[56:57]
	v_cndmask_b32_e64 v179, 0, v179, s[58:59]
	v_cndmask_b32_e64 v180, 0, v180, s[60:61]
	v_cndmask_b32_e64 v181, 0, v181, s[62:63]
	v_cndmask_b32_e64 v182, 0, v182, s[64:65]
	v_cndmask_b32_e64 v183, 0, v183, s[66:67]
	v_cvt_pk_f16_f32 v184, v176, v177
	v_cvt_pk_f16_f32 v185, v178, v179
	v_cvt_pk_f16_f32 v186, v180, v181
	v_cvt_pk_f16_f32 v187, v182, v183
	s_nop 1
	v_mfma_f32_16x16x32_f16 v[112:115], v[144:147], v[184:187], v[112:115]
	v_mfma_f32_16x16x32_f16 v[116:119], v[148:151], v[184:187], v[116:119]
	v_mfma_f32_16x16x32_f16 v[120:123], v[152:155], v[184:187], v[120:123]
	v_mfma_f32_16x16x32_f16 v[124:127], v[156:159], v[184:187], v[124:127]
	v_mfma_f32_16x16x32_f16 v[128:131], v[144:147], v[92:95], 0
	v_mfma_f32_16x16x32_f16 v[132:135], v[148:151], v[92:95], 0
	v_mfma_f32_16x16x32_f16 v[136:139], v[152:155], v[92:95], 0
	v_mfma_f32_16x16x32_f16 v[140:143], v[156:159], v[92:95], 0
	s_branch .Lmy_s2_kend19

.Lmy_s2_diag26:
	ds_read_b64 v[234:235], v216 offset:32768
	ds_read_b64 v[236:237], v217 offset:32768
	ds_read_b64 v[238:239], v218 offset:32768
	ds_read_b64 v[240:241], v219 offset:32768
	s_waitcnt lgkmcnt(4)
	v_fma_f32 v232, v232, s51, v189
	v_exp_f32_e32 v232, v232
	s_nop 0
	v_pk_mul_f32 v[224:225], v[224:225], v[232:233] op_sel_hi:[1,0]
	v_pk_mul_f32 v[226:227], v[226:227], v[232:233] op_sel_hi:[1,0]
	v_pk_mul_f32 v[228:229], v[228:229], v[232:233] op_sel_hi:[1,0]
	v_pk_mul_f32 v[230:231], v[230:231], v[232:233] op_sel_hi:[1,0]
	v_pk_mul_f32 v[224:225], v[84:85], v[224:225]
	v_pk_mul_f32 v[226:227], v[86:87], v[226:227]
	v_pk_mul_f32 v[228:229], v[88:89], v[228:229]
	v_pk_mul_f32 v[230:231], v[90:91], v[230:231]
	v_cndmask_b32_e64 v224, 0, v224, s[52:53]
	v_cndmask_b32_e64 v225, 0, v225, s[54:55]
	v_cndmask_b32_e64 v226, 0, v226, s[56:57]
	v_cndmask_b32_e64 v227, 0, v227, s[58:59]
	v_cndmask_b32_e64 v228, 0, v228, s[60:61]
	v_cndmask_b32_e64 v229, 0, v229, s[62:63]
	v_cndmask_b32_e64 v230, 0, v230, s[64:65]
	v_cndmask_b32_e64 v231, 0, v231, s[66:67]
	v_cvt_pk_f16_f32 v184, v224, v225
	v_cvt_pk_f16_f32 v185, v226, v227
	v_cvt_pk_f16_f32 v186, v228, v229
	v_cvt_pk_f16_f32 v187, v230, v231
	s_nop 1
	v_mfma_f32_16x16x32_f16 v[112:115], v[160:163], v[184:187], v[112:115]
	v_mfma_f32_16x16x32_f16 v[116:119], v[164:167], v[184:187], v[116:119]
	v_mfma_f32_16x16x32_f16 v[120:123], v[168:171], v[184:187], v[120:123]
	v_mfma_f32_16x16x32_f16 v[124:127], v[172:175], v[184:187], v[124:127]
	v_mfma_f32_16x16x32_f16 v[128:131], v[160:163], v[92:95], 0
	v_mfma_f32_16x16x32_f16 v[132:135], v[164:167], v[92:95], 0
	v_mfma_f32_16x16x32_f16 v[136:139], v[168:171], v[92:95], 0
	v_mfma_f32_16x16x32_f16 v[140:143], v[172:175], v[92:95], 0
	s_branch .Lmy_s2_kend19
.Lmy_s2_knext27:
.Lmy_s2_kend19:
	v_readlane_b32 s46, v11, 2
	v_readlane_b32 s47, v12, 2
	v_exp_f32_e32 v190, v189
	s_waitcnt lgkmcnt(0)
	s_nop 7
	v_cvt_f32_f16_e32 v198, v234
	v_cvt_f32_f16_sdwa v199, v234 dst_sel:DWORD dst_unused:UNUSED_PAD src0_sel:WORD_1
	v_cvt_f32_f16_e32 v200, v235
	v_cvt_f32_f16_sdwa v201, v235 dst_sel:DWORD dst_unused:UNUSED_PAD src0_sel:WORD_1
	v_pk_fma_f32 v[192:193], v[190:191], v[96:97], v[112:113] op_sel_hi:[0,1,1]
	v_pk_fma_f32 v[194:195], v[190:191], v[98:99], v[114:115] op_sel_hi:[0,1,1]
	v_pk_mul_f32 v[192:193], v[192:193], s[46:47] op_sel:[0,1] op_sel_hi:[1,1]
	v_pk_mul_f32 v[194:195], v[194:195], s[46:47] op_sel:[0,1] op_sel_hi:[1,1]
	v_pk_fma_f32 v[192:193], s[46:47], v[128:129], v[192:193] op_sel_hi:[0,1,1]
	v_pk_fma_f32 v[194:195], s[46:47], v[130:131], v[194:195] op_sel_hi:[0,1,1]
	v_pk_mul_f32 v[192:193], v[192:193], v[198:199]
	v_pk_mul_f32 v[194:195], v[194:195], v[200:201]
	v_pk_fma_f32 v[250:251], v[192:193], v[192:193], v[250:251]
	v_pk_fma_f32 v[250:251], v[194:195], v[194:195], v[250:251]
	v_cvt_pk_f16_f32 v196, v192, v193
	v_cvt_pk_f16_f32 v197, v194, v195
	global_store_dwordx2 v242, v[196:197], s[38:39]
	v_cvt_f32_f16_e32 v198, v236
	v_cvt_f32_f16_sdwa v199, v236 dst_sel:DWORD dst_unused:UNUSED_PAD src0_sel:WORD_1
	v_cvt_f32_f16_e32 v200, v237
	v_cvt_f32_f16_sdwa v201, v237 dst_sel:DWORD dst_unused:UNUSED_PAD src0_sel:WORD_1
	v_pk_fma_f32 v[192:193], v[190:191], v[100:101], v[116:117] op_sel_hi:[0,1,1]
	v_pk_fma_f32 v[194:195], v[190:191], v[102:103], v[118:119] op_sel_hi:[0,1,1]
	v_pk_mul_f32 v[192:193], v[192:193], s[46:47] op_sel:[0,1] op_sel_hi:[1,1]
	v_pk_mul_f32 v[194:195], v[194:195], s[46:47] op_sel:[0,1] op_sel_hi:[1,1]
	v_pk_fma_f32 v[192:193], s[46:47], v[132:133], v[192:193] op_sel_hi:[0,1,1]
	v_pk_fma_f32 v[194:195], s[46:47], v[134:135], v[194:195] op_sel_hi:[0,1,1]
	v_pk_mul_f32 v[192:193], v[192:193], v[198:199]
	v_pk_mul_f32 v[194:195], v[194:195], v[200:201]
	v_pk_fma_f32 v[250:251], v[192:193], v[192:193], v[250:251]
	v_pk_fma_f32 v[250:251], v[194:195], v[194:195], v[250:251]
	v_cvt_pk_f16_f32 v196, v192, v193
	v_cvt_pk_f16_f32 v197, v194, v195
	global_store_dwordx2 v242, v[196:197], s[38:39] offset:32
	v_cvt_f32_f16_e32 v198, v238
	v_cvt_f32_f16_sdwa v199, v238 dst_sel:DWORD dst_unused:UNUSED_PAD src0_sel:WORD_1
	v_cvt_f32_f16_e32 v200, v239
	v_cvt_f32_f16_sdwa v201, v239 dst_sel:DWORD dst_unused:UNUSED_PAD src0_sel:WORD_1
	v_pk_fma_f32 v[192:193], v[190:191], v[104:105], v[120:121] op_sel_hi:[0,1,1]
	v_pk_fma_f32 v[194:195], v[190:191], v[106:107], v[122:123] op_sel_hi:[0,1,1]
	v_pk_mul_f32 v[192:193], v[192:193], s[46:47] op_sel:[0,1] op_sel_hi:[1,1]
	v_pk_mul_f32 v[194:195], v[194:195], s[46:47] op_sel:[0,1] op_sel_hi:[1,1]
	v_pk_fma_f32 v[192:193], s[46:47], v[136:137], v[192:193] op_sel_hi:[0,1,1]
	v_pk_fma_f32 v[194:195], s[46:47], v[138:139], v[194:195] op_sel_hi:[0,1,1]
	v_pk_mul_f32 v[192:193], v[192:193], v[198:199]
	v_pk_mul_f32 v[194:195], v[194:195], v[200:201]
	v_pk_fma_f32 v[250:251], v[192:193], v[192:193], v[250:251]
	v_pk_fma_f32 v[250:251], v[194:195], v[194:195], v[250:251]
	v_cvt_pk_f16_f32 v196, v192, v193
	v_cvt_pk_f16_f32 v197, v194, v195
	global_store_dwordx2 v242, v[196:197], s[38:39] offset:64
	v_cvt_f32_f16_e32 v198, v240
	v_cvt_f32_f16_sdwa v199, v240 dst_sel:DWORD dst_unused:UNUSED_PAD src0_sel:WORD_1
	v_cvt_f32_f16_e32 v200, v241
	v_cvt_f32_f16_sdwa v201, v241 dst_sel:DWORD dst_unused:UNUSED_PAD src0_sel:WORD_1
	v_pk_fma_f32 v[192:193], v[190:191], v[108:109], v[124:125] op_sel_hi:[0,1,1]
	v_pk_fma_f32 v[194:195], v[190:191], v[110:111], v[126:127] op_sel_hi:[0,1,1]
	v_pk_mul_f32 v[192:193], v[192:193], s[46:47] op_sel:[0,1] op_sel_hi:[1,1]
	v_pk_mul_f32 v[194:195], v[194:195], s[46:47] op_sel:[0,1] op_sel_hi:[1,1]
	v_pk_fma_f32 v[192:193], s[46:47], v[140:141], v[192:193] op_sel_hi:[0,1,1]
	v_pk_fma_f32 v[194:195], s[46:47], v[142:143], v[194:195] op_sel_hi:[0,1,1]
	v_pk_mul_f32 v[192:193], v[192:193], v[198:199]
	v_pk_mul_f32 v[194:195], v[194:195], v[200:201]
	v_pk_fma_f32 v[250:251], v[192:193], v[192:193], v[250:251]
	v_pk_fma_f32 v[250:251], v[194:195], v[194:195], v[250:251]
	v_cvt_pk_f16_f32 v196, v192, v193
	v_cvt_pk_f16_f32 v197, v194, v195
	global_store_dwordx2 v242, v[196:197], s[38:39] offset:96
	s_add_u32 s38, s38, 0x80
	s_addc_u32 s39, s39, 0
	s_waitcnt vmcnt(15)
	s_waitcnt lgkmcnt(0)
	s_barrier
	ds_read_b128 v[144:147], v16 offset:16384
	ds_read_b128 v[148:151], v16 offset:20480
	ds_read_b128 v[152:155], v16 offset:24576
	ds_read_b128 v[156:159], v16 offset:28672
	ds_read_b32 v189, v36 offset:49152
	s_add_u32 m0, s43, 0x19000
	s_nop 0
	global_load_lds_dwordx4 v4, s[30:31]
	s_add_u32 m0, s43, 0x1d000
	s_nop 0
	global_load_lds_dwordx4 v6, s[32:33]
	s_add_u32 m0, s43, 0x21000
	s_nop 0
	global_load_lds_dwordx4 v8, s[34:35]
	s_add_u32 m0, s43, 0x1b000
	s_nop 0
	global_load_lds_dwordx4 v5, s[30:31]
	s_add_u32 m0, s43, 0x1f000
	s_nop 0
	global_load_lds_dwordx4 v7, s[32:33]
	s_add_u32 m0, s43, 0x23000
	s_nop 0
	global_load_lds_dwordx4 v9, s[34:35]
	s_add_u32 m0, s44, 0x25000
	s_nop 0
	global_load_lds_dword v10, s[36:37]
	s_add_u32 s30, s30, 0x80000
	s_addc_u32 s31, s31, 0
	s_add_u32 s32, s32, 0x4000
	s_addc_u32 s33, s33, 0
	s_add_u32 s34, s34, 0x80
	s_addc_u32 s35, s35, 0
	s_add_u32 s36, s36, 0x4000
	s_addc_u32 s37, s37, 0
	ds_read_b128 v[160:163], v17 offset:16384
	ds_read_b128 v[164:167], v17 offset:20480
	ds_read_b128 v[168:171], v17 offset:24576
	ds_read_b128 v[172:175], v17 offset:28672
	s_waitcnt lgkmcnt(4)
	v_mfma_f32_16x16x32_f16 v[96:99], v[144:147], v[44:47], 0
	v_mfma_f32_16x16x32_f16 v[100:103], v[148:151], v[44:47], 0
	v_mfma_f32_16x16x32_f16 v[104:107], v[152:155], v[44:47], 0
	v_mfma_f32_16x16x32_f16 v[108:111], v[156:159], v[44:47], 0
	ds_read_b128 v[144:147], v18 offset:16384
	ds_read_b128 v[148:151], v18 offset:20480
	ds_read_b128 v[152:155], v18 offset:24576
	ds_read_b128 v[156:159], v18 offset:28672
	s_waitcnt lgkmcnt(4)
	v_mfma_f32_16x16x32_f16 v[96:99], v[160:163], v[48:51], v[96:99]
	v_mfma_f32_16x16x32_f16 v[100:103], v[164:167], v[48:51], v[100:103]
	v_mfma_f32_16x16x32_f16 v[104:107], v[168:171], v[48:51], v[104:107]
	v_mfma_f32_16x16x32_f16 v[108:111], v[172:175], v[48:51], v[108:111]
	ds_read_b128 v[160:163], v19 offset:16384
	ds_read_b128 v[164:167], v19 offset:20480
	ds_read_b128 v[168:171], v19 offset:24576
	ds_read_b128 v[172:175], v19 offset:28672
	s_waitcnt lgkmcnt(4)
	v_mfma_f32_16x16x32_f16 v[96:99], v[144:147], v[52:55], v[96:99]
	v_mfma_f32_16x16x32_f16 v[100:103], v[148:151], v[52:55], v[100:103]
	v_mfma_f32_16x16x32_f16 v[104:107], v[152:155], v[52:55], v[104:107]
	v_mfma_f32_16x16x32_f16 v[108:111], v[156:159], v[52:55], v[108:111]
	ds_read_b128 v[176:179], v38 offset:49664
	ds_read_b128 v[180:183], v38 offset:49680
	ds_read_b32 v188, v38 offset:49152
	ds_read_b128 v[144:147], v16 offset:0
	ds_read_b128 v[148:151], v16 offset:4096
	ds_read_b128 v[152:155], v16 offset:8192
	ds_read_b128 v[156:159], v16 offset:12288
	s_waitcnt lgkmcnt(7)
	v_mfma_f32_16x16x32_f16 v[96:99], v[160:163], v[56:59], v[96:99]
	v_mfma_f32_16x16x32_f16 v[100:103], v[164:167], v[56:59], v[100:103]
	v_mfma_f32_16x16x32_f16 v[104:107], v[168:171], v[56:59], v[104:107]
	v_mfma_f32_16x16x32_f16 v[108:111], v[172:175], v[56:59], v[108:111]
	v_mul_f32_e32 v189, 0x3fb8aa3b, v189
	s_cmp_lt_u32 s42, 0
	s_cbranch_scc1 .Lmy_s2_kend28
	s_cmp_eq_u32 s42, 0
	s_cbranch_scc1 .Lmy_s2_diag29
	ds_read_b128 v[224:227], v38 offset:49792
	ds_read_b128 v[228:231], v38 offset:49808
	ds_read_b32 v232, v38 offset:49280
	ds_read_b128 v[160:163], v17 offset:0
	ds_read_b128 v[164:167], v17 offset:4096
	ds_read_b128 v[168:171], v17 offset:8192
	ds_read_b128 v[172:175], v17 offset:12288
	s_waitcnt lgkmcnt(7)
	v_fma_f32 v188, v188, s51, v189
	v_exp_f32_e32 v188, v188
	s_nop 0
	v_pk_mul_f32 v[176:177], v[176:177], v[188:189] op_sel_hi:[1,0]
	v_pk_mul_f32 v[178:179], v[178:179], v[188:189] op_sel_hi:[1,0]
	v_pk_mul_f32 v[180:181], v[180:181], v[188:189] op_sel_hi:[1,0]
	v_pk_mul_f32 v[182:183], v[182:183], v[188:189] op_sel_hi:[1,0]
	v_pk_mul_f32 v[176:177], v[60:61], v[176:177]
	v_pk_mul_f32 v[178:179], v[62:63], v[178:179]
	v_pk_mul_f32 v[180:181], v[64:65], v[180:181]
	v_pk_mul_f32 v[182:183], v[66:67], v[182:183]
	v_cvt_pk_f16_f32 v184, v176, v177
	v_cvt_pk_f16_f32 v185, v178, v179
	v_cvt_pk_f16_f32 v186, v180, v181
	v_cvt_pk_f16_f32 v187, v182, v183
	s_nop 1
	v_mfma_f32_16x16x32_f16 v[112:115], v[144:147], v[184:187], 0
	v_mfma_f32_16x16x32_f16 v[116:119], v[148:151], v[184:187], 0
	v_mfma_f32_16x16x32_f16 v[120:123], v[152:155], v[184:187], 0
	v_mfma_f32_16x16x32_f16 v[124:127], v[156:159], v[184:187], 0
	s_branch .Lmy_s2_knext30

.Lmy_s2_knext36:
.Lmy_s2_kend28:
	v_readlane_b32 s46, v11, 3
	v_readlane_b32 s47, v12, 3
	v_exp_f32_e32 v190, v189
	s_waitcnt lgkmcnt(0)
	s_nop 7
	v_cvt_f32_f16_e32 v198, v234
	v_cvt_f32_f16_sdwa v199, v234 dst_sel:DWORD dst_unused:UNUSED_PAD src0_sel:WORD_1
	v_cvt_f32_f16_e32 v200, v235
	v_cvt_f32_f16_sdwa v201, v235 dst_sel:DWORD dst_unused:UNUSED_PAD src0_sel:WORD_1
	v_pk_fma_f32 v[192:193], v[190:191], v[96:97], v[112:113] op_sel_hi:[0,1,1]
	v_pk_fma_f32 v[194:195], v[190:191], v[98:99], v[114:115] op_sel_hi:[0,1,1]
	v_pk_mul_f32 v[192:193], v[192:193], s[46:47] op_sel:[0,1] op_sel_hi:[1,1]
	v_pk_mul_f32 v[194:195], v[194:195], s[46:47] op_sel:[0,1] op_sel_hi:[1,1]
	v_pk_fma_f32 v[192:193], s[46:47], v[128:129], v[192:193] op_sel_hi:[0,1,1]
	v_pk_fma_f32 v[194:195], s[46:47], v[130:131], v[194:195] op_sel_hi:[0,1,1]
	v_pk_mul_f32 v[192:193], v[192:193], v[198:199]
	v_pk_mul_f32 v[194:195], v[194:195], v[200:201]
	v_pk_fma_f32 v[250:251], v[192:193], v[192:193], v[250:251]
	v_pk_fma_f32 v[250:251], v[194:195], v[194:195], v[250:251]
	v_cvt_pk_f16_f32 v196, v192, v193
	v_cvt_pk_f16_f32 v197, v194, v195
	global_store_dwordx2 v242, v[196:197], s[38:39]
	v_cvt_f32_f16_e32 v198, v236
	v_cvt_f32_f16_sdwa v199, v236 dst_sel:DWORD dst_unused:UNUSED_PAD src0_sel:WORD_1
	v_cvt_f32_f16_e32 v200, v237
	v_cvt_f32_f16_sdwa v201, v237 dst_sel:DWORD dst_unused:UNUSED_PAD src0_sel:WORD_1
	v_pk_fma_f32 v[192:193], v[190:191], v[100:101], v[116:117] op_sel_hi:[0,1,1]
	v_pk_fma_f32 v[194:195], v[190:191], v[102:103], v[118:119] op_sel_hi:[0,1,1]
	v_pk_mul_f32 v[192:193], v[192:193], s[46:47] op_sel:[0,1] op_sel_hi:[1,1]
	v_pk_mul_f32 v[194:195], v[194:195], s[46:47] op_sel:[0,1] op_sel_hi:[1,1]
	v_pk_fma_f32 v[192:193], s[46:47], v[132:133], v[192:193] op_sel_hi:[0,1,1]
	v_pk_fma_f32 v[194:195], s[46:47], v[134:135], v[194:195] op_sel_hi:[0,1,1]
	v_pk_mul_f32 v[192:193], v[192:193], v[198:199]
	v_pk_mul_f32 v[194:195], v[194:195], v[200:201]
	v_pk_fma_f32 v[250:251], v[192:193], v[192:193], v[250:251]
	v_pk_fma_f32 v[250:251], v[194:195], v[194:195], v[250:251]
	v_cvt_pk_f16_f32 v196, v192, v193
	v_cvt_pk_f16_f32 v197, v194, v195
	global_store_dwordx2 v242, v[196:197], s[38:39] offset:32
	v_cvt_f32_f16_e32 v198, v238
	v_cvt_f32_f16_sdwa v199, v238 dst_sel:DWORD dst_unused:UNUSED_PAD src0_sel:WORD_1
	v_cvt_f32_f16_e32 v200, v239
	v_cvt_f32_f16_sdwa v201, v239 dst_sel:DWORD dst_unused:UNUSED_PAD src0_sel:WORD_1
	v_pk_fma_f32 v[192:193], v[190:191], v[104:105], v[120:121] op_sel_hi:[0,1,1]
	v_pk_fma_f32 v[194:195], v[190:191], v[106:107], v[122:123] op_sel_hi:[0,1,1]
	v_pk_mul_f32 v[192:193], v[192:193], s[46:47] op_sel:[0,1] op_sel_hi:[1,1]
	v_pk_mul_f32 v[194:195], v[194:195], s[46:47] op_sel:[0,1] op_sel_hi:[1,1]
	v_pk_fma_f32 v[192:193], s[46:47], v[136:137], v[192:193] op_sel_hi:[0,1,1]
	v_pk_fma_f32 v[194:195], s[46:47], v[138:139], v[194:195] op_sel_hi:[0,1,1]
	v_pk_mul_f32 v[192:193], v[192:193], v[198:199]
	v_pk_mul_f32 v[194:195], v[194:195], v[200:201]
	v_pk_fma_f32 v[250:251], v[192:193], v[192:193], v[250:251]
	v_pk_fma_f32 v[250:251], v[194:195], v[194:195], v[250:251]
	v_cvt_pk_f16_f32 v196, v192, v193
	v_cvt_pk_f16_f32 v197, v194, v195
	global_store_dwordx2 v242, v[196:197], s[38:39] offset:64
	v_cvt_f32_f16_e32 v198, v240
	v_cvt_f32_f16_sdwa v199, v240 dst_sel:DWORD dst_unused:UNUSED_PAD src0_sel:WORD_1
	v_cvt_f32_f16_e32 v200, v241
	v_cvt_f32_f16_sdwa v201, v241 dst_sel:DWORD dst_unused:UNUSED_PAD src0_sel:WORD_1
	v_pk_fma_f32 v[192:193], v[190:191], v[108:109], v[124:125] op_sel_hi:[0,1,1]
	v_pk_fma_f32 v[194:195], v[190:191], v[110:111], v[126:127] op_sel_hi:[0,1,1]
	v_pk_mul_f32 v[192:193], v[192:193], s[46:47] op_sel:[0,1] op_sel_hi:[1,1]
	v_pk_mul_f32 v[194:195], v[194:195], s[46:47] op_sel:[0,1] op_sel_hi:[1,1]
	v_pk_fma_f32 v[192:193], s[46:47], v[140:141], v[192:193] op_sel_hi:[0,1,1]
	v_pk_fma_f32 v[194:195], s[46:47], v[142:143], v[194:195] op_sel_hi:[0,1,1]
	v_pk_mul_f32 v[192:193], v[192:193], v[198:199]
	v_pk_mul_f32 v[194:195], v[194:195], v[200:201]
	v_pk_fma_f32 v[250:251], v[192:193], v[192:193], v[250:251]
	v_pk_fma_f32 v[250:251], v[194:195], v[194:195], v[250:251]
	v_cvt_pk_f16_f32 v196, v192, v193
	v_cvt_pk_f16_f32 v197, v194, v195
	global_store_dwordx2 v242, v[196:197], s[38:39] offset:96
	s_add_u32 s38, s38, 0x80
	s_addc_u32 s39, s39, 0
	s_waitcnt vmcnt(15)
	s_waitcnt lgkmcnt(0)
	s_barrier
	ds_read_b128 v[144:147], v20 offset:16384
	ds_read_b128 v[148:151], v20 offset:20480
	ds_read_b128 v[152:155], v20 offset:24576
	ds_read_b128 v[156:159], v20 offset:28672
	ds_read_b32 v189, v37 offset:49152
	s_add_u32 m0, s43, 0x0
	s_nop 0
	global_load_lds_dwordx4 v4, s[30:31]
	s_add_u32 m0, s43, 0x4000
	s_nop 0
	global_load_lds_dwordx4 v6, s[32:33]
	s_add_u32 m0, s43, 0x8000
	s_nop 0
	global_load_lds_dwordx4 v8, s[34:35]
	s_add_u32 m0, s43, 0x2000
	s_nop 0
	global_load_lds_dwordx4 v5, s[30:31]
	s_add_u32 m0, s43, 0x6000
	s_nop 0
	global_load_lds_dwordx4 v7, s[32:33]
	s_add_u32 m0, s43, 0xa000
	s_nop 0
	global_load_lds_dwordx4 v9, s[34:35]
	s_add_u32 m0, s44, 0xc000
	s_nop 0
	global_load_lds_dword v10, s[36:37]
	s_add_u32 s30, s30, 0x80000
	s_addc_u32 s31, s31, 0
	s_add_u32 s32, s32, 0x4000
	s_addc_u32 s33, s33, 0
	s_add_u32 s34, s34, 0x80
	s_addc_u32 s35, s35, 0
	s_add_u32 s36, s36, 0x4000
	s_addc_u32 s37, s37, 0
	ds_read_b128 v[160:163], v21 offset:16384
	ds_read_b128 v[164:167], v21 offset:20480
	ds_read_b128 v[168:171], v21 offset:24576
	ds_read_b128 v[172:175], v21 offset:28672
	s_waitcnt lgkmcnt(4)
	v_mfma_f32_16x16x32_f16 v[96:99], v[144:147], v[44:47], 0
	v_mfma_f32_16x16x32_f16 v[100:103], v[148:151], v[44:47], 0
	v_mfma_f32_16x16x32_f16 v[104:107], v[152:155], v[44:47], 0
	v_mfma_f32_16x16x32_f16 v[108:111], v[156:159], v[44:47], 0
	ds_read_b128 v[144:147], v22 offset:16384
	ds_read_b128 v[148:151], v22 offset:20480
	ds_read_b128 v[152:155], v22 offset:24576
	ds_read_b128 v[156:159], v22 offset:28672
	s_waitcnt lgkmcnt(4)
	v_mfma_f32_16x16x32_f16 v[96:99], v[160:163], v[48:51], v[96:99]
	v_mfma_f32_16x16x32_f16 v[100:103], v[164:167], v[48:51], v[100:103]
	v_mfma_f32_16x16x32_f16 v[104:107], v[168:171], v[48:51], v[104:107]
	v_mfma_f32_16x16x32_f16 v[108:111], v[172:175], v[48:51], v[108:111]
	ds_read_b128 v[160:163], v23 offset:16384
	ds_read_b128 v[164:167], v23 offset:20480
	ds_read_b128 v[168:171], v23 offset:24576
	ds_read_b128 v[172:175], v23 offset:28672
	s_waitcnt lgkmcnt(4)
	v_mfma_f32_16x16x32_f16 v[96:99], v[144:147], v[52:55], v[96:99]
	v_mfma_f32_16x16x32_f16 v[100:103], v[148:151], v[52:55], v[100:103]
	v_mfma_f32_16x16x32_f16 v[104:107], v[152:155], v[52:55], v[104:107]
	v_mfma_f32_16x16x32_f16 v[108:111], v[156:159], v[52:55], v[108:111]
	ds_read_b128 v[176:179], v39 offset:49664
	ds_read_b128 v[180:183], v39 offset:49680
	ds_read_b32 v188, v39 offset:49152
	ds_read_b128 v[144:147], v20 offset:0
	ds_read_b128 v[148:151], v20 offset:4096
	ds_read_b128 v[152:155], v20 offset:8192
	ds_read_b128 v[156:159], v20 offset:12288
	s_waitcnt lgkmcnt(7)
	v_mfma_f32_16x16x32_f16 v[96:99], v[160:163], v[56:59], v[96:99]
	v_mfma_f32_16x16x32_f16 v[100:103], v[164:167], v[56:59], v[100:103]
	v_mfma_f32_16x16x32_f16 v[104:107], v[168:171], v[56:59], v[104:107]
	v_mfma_f32_16x16x32_f16 v[108:111], v[172:175], v[56:59], v[108:111]
	v_mul_f32_e32 v189, 0x3fb8aa3b, v189
	s_cmp_lt_u32 s42, 0
	s_cbranch_scc1 .Lmy_s2_kend37
	s_cmp_eq_u32 s42, 0
	s_cbranch_scc1 .Lmy_s2_diag38
	ds_read_b128 v[224:227], v39 offset:49792
	ds_read_b128 v[228:231], v39 offset:49808
	ds_read_b32 v232, v39 offset:49280
	ds_read_b128 v[160:163], v21 offset:0
	ds_read_b128 v[164:167], v21 offset:4096
	ds_read_b128 v[168:171], v21 offset:8192
	ds_read_b128 v[172:175], v21 offset:12288
	s_waitcnt lgkmcnt(7)
	v_fma_f32 v188, v188, s51, v189
	v_exp_f32_e32 v188, v188
	s_nop 0
	v_pk_mul_f32 v[176:177], v[176:177], v[188:189] op_sel_hi:[1,0]
	v_pk_mul_f32 v[178:179], v[178:179], v[188:189] op_sel_hi:[1,0]
	v_pk_mul_f32 v[180:181], v[180:181], v[188:189] op_sel_hi:[1,0]
	v_pk_mul_f32 v[182:183], v[182:183], v[188:189] op_sel_hi:[1,0]
	v_pk_mul_f32 v[176:177], v[60:61], v[176:177]
	v_pk_mul_f32 v[178:179], v[62:63], v[178:179]
	v_pk_mul_f32 v[180:181], v[64:65], v[180:181]
	v_pk_mul_f32 v[182:183], v[66:67], v[182:183]
	v_cvt_pk_f16_f32 v184, v176, v177
	v_cvt_pk_f16_f32 v185, v178, v179
	v_cvt_pk_f16_f32 v186, v180, v181
	v_cvt_pk_f16_f32 v187, v182, v183
	s_nop 1
	v_mfma_f32_16x16x32_f16 v[112:115], v[144:147], v[184:187], 0
	v_mfma_f32_16x16x32_f16 v[116:119], v[148:151], v[184:187], 0
	v_mfma_f32_16x16x32_f16 v[120:123], v[152:155], v[184:187], 0
	v_mfma_f32_16x16x32_f16 v[124:127], v[156:159], v[184:187], 0
	s_branch .Lmy_s2_knext39

.Lmy_s2_knext45:
.Lmy_s2_kend37:
	v_readlane_b32 s46, v11, 4
	v_readlane_b32 s47, v12, 4
	v_exp_f32_e32 v190, v189
	s_waitcnt lgkmcnt(0)
	s_nop 7
	v_cvt_f32_f16_e32 v198, v234
	v_cvt_f32_f16_sdwa v199, v234 dst_sel:DWORD dst_unused:UNUSED_PAD src0_sel:WORD_1
	v_cvt_f32_f16_e32 v200, v235
	v_cvt_f32_f16_sdwa v201, v235 dst_sel:DWORD dst_unused:UNUSED_PAD src0_sel:WORD_1
	v_pk_fma_f32 v[192:193], v[190:191], v[96:97], v[112:113] op_sel_hi:[0,1,1]
	v_pk_fma_f32 v[194:195], v[190:191], v[98:99], v[114:115] op_sel_hi:[0,1,1]
	v_pk_mul_f32 v[192:193], v[192:193], s[46:47] op_sel:[0,1] op_sel_hi:[1,1]
	v_pk_mul_f32 v[194:195], v[194:195], s[46:47] op_sel:[0,1] op_sel_hi:[1,1]
	v_pk_fma_f32 v[192:193], s[46:47], v[128:129], v[192:193] op_sel_hi:[0,1,1]
	v_pk_fma_f32 v[194:195], s[46:47], v[130:131], v[194:195] op_sel_hi:[0,1,1]
	v_pk_mul_f32 v[192:193], v[192:193], v[198:199]
	v_pk_mul_f32 v[194:195], v[194:195], v[200:201]
	v_pk_fma_f32 v[250:251], v[192:193], v[192:193], v[250:251]
	v_pk_fma_f32 v[250:251], v[194:195], v[194:195], v[250:251]
	v_cvt_pk_f16_f32 v196, v192, v193
	v_cvt_pk_f16_f32 v197, v194, v195
	global_store_dwordx2 v242, v[196:197], s[38:39]
	v_cvt_f32_f16_e32 v198, v236
	v_cvt_f32_f16_sdwa v199, v236 dst_sel:DWORD dst_unused:UNUSED_PAD src0_sel:WORD_1
	v_cvt_f32_f16_e32 v200, v237
	v_cvt_f32_f16_sdwa v201, v237 dst_sel:DWORD dst_unused:UNUSED_PAD src0_sel:WORD_1
	v_pk_fma_f32 v[192:193], v[190:191], v[100:101], v[116:117] op_sel_hi:[0,1,1]
	v_pk_fma_f32 v[194:195], v[190:191], v[102:103], v[118:119] op_sel_hi:[0,1,1]
	v_pk_mul_f32 v[192:193], v[192:193], s[46:47] op_sel:[0,1] op_sel_hi:[1,1]
	v_pk_mul_f32 v[194:195], v[194:195], s[46:47] op_sel:[0,1] op_sel_hi:[1,1]
	v_pk_fma_f32 v[192:193], s[46:47], v[132:133], v[192:193] op_sel_hi:[0,1,1]
	v_pk_fma_f32 v[194:195], s[46:47], v[134:135], v[194:195] op_sel_hi:[0,1,1]
	v_pk_mul_f32 v[192:193], v[192:193], v[198:199]
	v_pk_mul_f32 v[194:195], v[194:195], v[200:201]
	v_pk_fma_f32 v[250:251], v[192:193], v[192:193], v[250:251]
	v_pk_fma_f32 v[250:251], v[194:195], v[194:195], v[250:251]
	v_cvt_pk_f16_f32 v196, v192, v193
	v_cvt_pk_f16_f32 v197, v194, v195
	global_store_dwordx2 v242, v[196:197], s[38:39] offset:32
	v_cvt_f32_f16_e32 v198, v238
	v_cvt_f32_f16_sdwa v199, v238 dst_sel:DWORD dst_unused:UNUSED_PAD src0_sel:WORD_1
	v_cvt_f32_f16_e32 v200, v239
	v_cvt_f32_f16_sdwa v201, v239 dst_sel:DWORD dst_unused:UNUSED_PAD src0_sel:WORD_1
	v_pk_fma_f32 v[192:193], v[190:191], v[104:105], v[120:121] op_sel_hi:[0,1,1]
	v_pk_fma_f32 v[194:195], v[190:191], v[106:107], v[122:123] op_sel_hi:[0,1,1]
	v_pk_mul_f32 v[192:193], v[192:193], s[46:47] op_sel:[0,1] op_sel_hi:[1,1]
	v_pk_mul_f32 v[194:195], v[194:195], s[46:47] op_sel:[0,1] op_sel_hi:[1,1]
	v_pk_fma_f32 v[192:193], s[46:47], v[136:137], v[192:193] op_sel_hi:[0,1,1]
	v_pk_fma_f32 v[194:195], s[46:47], v[138:139], v[194:195] op_sel_hi:[0,1,1]
	v_pk_mul_f32 v[192:193], v[192:193], v[198:199]
	v_pk_mul_f32 v[194:195], v[194:195], v[200:201]
	v_pk_fma_f32 v[250:251], v[192:193], v[192:193], v[250:251]
	v_pk_fma_f32 v[250:251], v[194:195], v[194:195], v[250:251]
	v_cvt_pk_f16_f32 v196, v192, v193
	v_cvt_pk_f16_f32 v197, v194, v195
	global_store_dwordx2 v242, v[196:197], s[38:39] offset:64
	v_cvt_f32_f16_e32 v198, v240
	v_cvt_f32_f16_sdwa v199, v240 dst_sel:DWORD dst_unused:UNUSED_PAD src0_sel:WORD_1
	v_cvt_f32_f16_e32 v200, v241
	v_cvt_f32_f16_sdwa v201, v241 dst_sel:DWORD dst_unused:UNUSED_PAD src0_sel:WORD_1
	v_pk_fma_f32 v[192:193], v[190:191], v[108:109], v[124:125] op_sel_hi:[0,1,1]
	v_pk_fma_f32 v[194:195], v[190:191], v[110:111], v[126:127] op_sel_hi:[0,1,1]
	v_pk_mul_f32 v[192:193], v[192:193], s[46:47] op_sel:[0,1] op_sel_hi:[1,1]
	v_pk_mul_f32 v[194:195], v[194:195], s[46:47] op_sel:[0,1] op_sel_hi:[1,1]
	v_pk_fma_f32 v[192:193], s[46:47], v[140:141], v[192:193] op_sel_hi:[0,1,1]
	v_pk_fma_f32 v[194:195], s[46:47], v[142:143], v[194:195] op_sel_hi:[0,1,1]
	v_pk_mul_f32 v[192:193], v[192:193], v[198:199]
	v_pk_mul_f32 v[194:195], v[194:195], v[200:201]
	v_pk_fma_f32 v[250:251], v[192:193], v[192:193], v[250:251]
	v_pk_fma_f32 v[250:251], v[194:195], v[194:195], v[250:251]
	v_cvt_pk_f16_f32 v196, v192, v193
	v_cvt_pk_f16_f32 v197, v194, v195
	global_store_dwordx2 v242, v[196:197], s[38:39] offset:96
	s_add_u32 s38, s38, 0x80
	s_addc_u32 s39, s39, 0
	s_waitcnt vmcnt(15)
	s_waitcnt lgkmcnt(0)
	s_barrier
	ds_read_b128 v[144:147], v212 offset:16384
	ds_read_b128 v[148:151], v212 offset:20480
	ds_read_b128 v[152:155], v212 offset:24576
	ds_read_b128 v[156:159], v212 offset:28672
	ds_read_b32 v189, v220 offset:49152
	s_add_u32 m0, s43, 0xc800
	s_nop 0
	global_load_lds_dwordx4 v4, s[30:31]
	s_add_u32 m0, s43, 0x10800
	s_nop 0
	global_load_lds_dwordx4 v6, s[32:33]
	s_add_u32 m0, s43, 0x14800
	s_nop 0
	global_load_lds_dwordx4 v8, s[34:35]
	s_add_u32 m0, s43, 0xe800
	s_nop 0
	global_load_lds_dwordx4 v5, s[30:31]
	s_add_u32 m0, s43, 0x12800
	s_nop 0
	global_load_lds_dwordx4 v7, s[32:33]
	s_add_u32 m0, s43, 0x16800
	s_nop 0
	global_load_lds_dwordx4 v9, s[34:35]
	s_add_u32 m0, s44, 0x18800
	s_nop 0
	global_load_lds_dword v10, s[36:37]
	s_add_u32 s30, s30, 0x80000
	s_addc_u32 s31, s31, 0
	s_add_u32 s32, s32, 0x4000
	s_addc_u32 s33, s33, 0
	s_add_u32 s34, s34, 0x80
	s_addc_u32 s35, s35, 0
	s_add_u32 s36, s36, 0x4000
	s_addc_u32 s37, s37, 0
	ds_read_b128 v[160:163], v213 offset:16384
	ds_read_b128 v[164:167], v213 offset:20480
	ds_read_b128 v[168:171], v213 offset:24576
	ds_read_b128 v[172:175], v213 offset:28672
	s_waitcnt lgkmcnt(4)
	v_mfma_f32_16x16x32_f16 v[96:99], v[144:147], v[44:47], 0
	v_mfma_f32_16x16x32_f16 v[100:103], v[148:151], v[44:47], 0
	v_mfma_f32_16x16x32_f16 v[104:107], v[152:155], v[44:47], 0
	v_mfma_f32_16x16x32_f16 v[108:111], v[156:159], v[44:47], 0
	ds_read_b128 v[144:147], v214 offset:16384
	ds_read_b128 v[148:151], v214 offset:20480
	ds_read_b128 v[152:155], v214 offset:24576
	ds_read_b128 v[156:159], v214 offset:28672
	s_waitcnt lgkmcnt(4)
	v_mfma_f32_16x16x32_f16 v[96:99], v[160:163], v[48:51], v[96:99]
	v_mfma_f32_16x16x32_f16 v[100:103], v[164:167], v[48:51], v[100:103]
	v_mfma_f32_16x16x32_f16 v[104:107], v[168:171], v[48:51], v[104:107]
	v_mfma_f32_16x16x32_f16 v[108:111], v[172:175], v[48:51], v[108:111]
	ds_read_b128 v[160:163], v215 offset:16384
	ds_read_b128 v[164:167], v215 offset:20480
	ds_read_b128 v[168:171], v215 offset:24576
	ds_read_b128 v[172:175], v215 offset:28672
	s_waitcnt lgkmcnt(4)
	v_mfma_f32_16x16x32_f16 v[96:99], v[144:147], v[52:55], v[96:99]
	v_mfma_f32_16x16x32_f16 v[100:103], v[148:151], v[52:55], v[100:103]
	v_mfma_f32_16x16x32_f16 v[104:107], v[152:155], v[52:55], v[104:107]
	v_mfma_f32_16x16x32_f16 v[108:111], v[156:159], v[52:55], v[108:111]
	ds_read_b128 v[176:179], v221 offset:49664
	ds_read_b128 v[180:183], v221 offset:49680
	ds_read_b32 v188, v221 offset:49152
	ds_read_b128 v[144:147], v212 offset:0
	ds_read_b128 v[148:151], v212 offset:4096
	ds_read_b128 v[152:155], v212 offset:8192
	ds_read_b128 v[156:159], v212 offset:12288
	s_waitcnt lgkmcnt(7)
	v_mfma_f32_16x16x32_f16 v[96:99], v[160:163], v[56:59], v[96:99]
	v_mfma_f32_16x16x32_f16 v[100:103], v[164:167], v[56:59], v[100:103]
	v_mfma_f32_16x16x32_f16 v[104:107], v[168:171], v[56:59], v[104:107]
	v_mfma_f32_16x16x32_f16 v[108:111], v[172:175], v[56:59], v[108:111]
	v_mul_f32_e32 v189, 0x3fb8aa3b, v189
	s_cmp_lt_u32 s42, 0
	s_cbranch_scc1 .Lmy_s2_kend46
	s_cmp_eq_u32 s42, 0
	s_cbranch_scc1 .Lmy_s2_diag47
	ds_read_b128 v[224:227], v221 offset:49792
	ds_read_b128 v[228:231], v221 offset:49808
	ds_read_b32 v232, v221 offset:49280
	ds_read_b128 v[160:163], v213 offset:0
	ds_read_b128 v[164:167], v213 offset:4096
	ds_read_b128 v[168:171], v213 offset:8192
	ds_read_b128 v[172:175], v213 offset:12288
	s_waitcnt lgkmcnt(7)
	v_fma_f32 v188, v188, s51, v189
	v_exp_f32_e32 v188, v188
	s_nop 0
	v_pk_mul_f32 v[176:177], v[176:177], v[188:189] op_sel_hi:[1,0]
	v_pk_mul_f32 v[178:179], v[178:179], v[188:189] op_sel_hi:[1,0]
	v_pk_mul_f32 v[180:181], v[180:181], v[188:189] op_sel_hi:[1,0]
	v_pk_mul_f32 v[182:183], v[182:183], v[188:189] op_sel_hi:[1,0]
	v_pk_mul_f32 v[176:177], v[60:61], v[176:177]
	v_pk_mul_f32 v[178:179], v[62:63], v[178:179]
	v_pk_mul_f32 v[180:181], v[64:65], v[180:181]
	v_pk_mul_f32 v[182:183], v[66:67], v[182:183]
	v_cvt_pk_f16_f32 v184, v176, v177
	v_cvt_pk_f16_f32 v185, v178, v179
	v_cvt_pk_f16_f32 v186, v180, v181
	v_cvt_pk_f16_f32 v187, v182, v183
	s_nop 1
	v_mfma_f32_16x16x32_f16 v[112:115], v[144:147], v[184:187], 0
	v_mfma_f32_16x16x32_f16 v[116:119], v[148:151], v[184:187], 0
	v_mfma_f32_16x16x32_f16 v[120:123], v[152:155], v[184:187], 0
	v_mfma_f32_16x16x32_f16 v[124:127], v[156:159], v[184:187], 0
	s_branch .Lmy_s2_knext48

.Lmy_s2_knext54:
.Lmy_s2_kend46:
	v_readlane_b32 s46, v11, 5
	v_readlane_b32 s47, v12, 5
	v_exp_f32_e32 v190, v189
	s_waitcnt lgkmcnt(0)
	s_nop 7
	v_cvt_f32_f16_e32 v198, v234
	v_cvt_f32_f16_sdwa v199, v234 dst_sel:DWORD dst_unused:UNUSED_PAD src0_sel:WORD_1
	v_cvt_f32_f16_e32 v200, v235
	v_cvt_f32_f16_sdwa v201, v235 dst_sel:DWORD dst_unused:UNUSED_PAD src0_sel:WORD_1
	v_pk_fma_f32 v[192:193], v[190:191], v[96:97], v[112:113] op_sel_hi:[0,1,1]
	v_pk_fma_f32 v[194:195], v[190:191], v[98:99], v[114:115] op_sel_hi:[0,1,1]
	v_pk_mul_f32 v[192:193], v[192:193], s[46:47] op_sel:[0,1] op_sel_hi:[1,1]
	v_pk_mul_f32 v[194:195], v[194:195], s[46:47] op_sel:[0,1] op_sel_hi:[1,1]
	v_pk_fma_f32 v[192:193], s[46:47], v[128:129], v[192:193] op_sel_hi:[0,1,1]
	v_pk_fma_f32 v[194:195], s[46:47], v[130:131], v[194:195] op_sel_hi:[0,1,1]
	v_pk_mul_f32 v[192:193], v[192:193], v[198:199]
	v_pk_mul_f32 v[194:195], v[194:195], v[200:201]
	v_pk_fma_f32 v[250:251], v[192:193], v[192:193], v[250:251]
	v_pk_fma_f32 v[250:251], v[194:195], v[194:195], v[250:251]
	v_cvt_pk_f16_f32 v196, v192, v193
	v_cvt_pk_f16_f32 v197, v194, v195
	global_store_dwordx2 v242, v[196:197], s[38:39]
	v_cvt_f32_f16_e32 v198, v236
	v_cvt_f32_f16_sdwa v199, v236 dst_sel:DWORD dst_unused:UNUSED_PAD src0_sel:WORD_1
	v_cvt_f32_f16_e32 v200, v237
	v_cvt_f32_f16_sdwa v201, v237 dst_sel:DWORD dst_unused:UNUSED_PAD src0_sel:WORD_1
	v_pk_fma_f32 v[192:193], v[190:191], v[100:101], v[116:117] op_sel_hi:[0,1,1]
	v_pk_fma_f32 v[194:195], v[190:191], v[102:103], v[118:119] op_sel_hi:[0,1,1]
	v_pk_mul_f32 v[192:193], v[192:193], s[46:47] op_sel:[0,1] op_sel_hi:[1,1]
	v_pk_mul_f32 v[194:195], v[194:195], s[46:47] op_sel:[0,1] op_sel_hi:[1,1]
	v_pk_fma_f32 v[192:193], s[46:47], v[132:133], v[192:193] op_sel_hi:[0,1,1]
	v_pk_fma_f32 v[194:195], s[46:47], v[134:135], v[194:195] op_sel_hi:[0,1,1]
	v_pk_mul_f32 v[192:193], v[192:193], v[198:199]
	v_pk_mul_f32 v[194:195], v[194:195], v[200:201]
	v_pk_fma_f32 v[250:251], v[192:193], v[192:193], v[250:251]
	v_pk_fma_f32 v[250:251], v[194:195], v[194:195], v[250:251]
	v_cvt_pk_f16_f32 v196, v192, v193
	v_cvt_pk_f16_f32 v197, v194, v195
	global_store_dwordx2 v242, v[196:197], s[38:39] offset:32
	v_cvt_f32_f16_e32 v198, v238
	v_cvt_f32_f16_sdwa v199, v238 dst_sel:DWORD dst_unused:UNUSED_PAD src0_sel:WORD_1
	v_cvt_f32_f16_e32 v200, v239
	v_cvt_f32_f16_sdwa v201, v239 dst_sel:DWORD dst_unused:UNUSED_PAD src0_sel:WORD_1
	v_pk_fma_f32 v[192:193], v[190:191], v[104:105], v[120:121] op_sel_hi:[0,1,1]
	v_pk_fma_f32 v[194:195], v[190:191], v[106:107], v[122:123] op_sel_hi:[0,1,1]
	v_pk_mul_f32 v[192:193], v[192:193], s[46:47] op_sel:[0,1] op_sel_hi:[1,1]
	v_pk_mul_f32 v[194:195], v[194:195], s[46:47] op_sel:[0,1] op_sel_hi:[1,1]
	v_pk_fma_f32 v[192:193], s[46:47], v[136:137], v[192:193] op_sel_hi:[0,1,1]
	v_pk_fma_f32 v[194:195], s[46:47], v[138:139], v[194:195] op_sel_hi:[0,1,1]
	v_pk_mul_f32 v[192:193], v[192:193], v[198:199]
	v_pk_mul_f32 v[194:195], v[194:195], v[200:201]
	v_pk_fma_f32 v[250:251], v[192:193], v[192:193], v[250:251]
	v_pk_fma_f32 v[250:251], v[194:195], v[194:195], v[250:251]
	v_cvt_pk_f16_f32 v196, v192, v193
	v_cvt_pk_f16_f32 v197, v194, v195
	global_store_dwordx2 v242, v[196:197], s[38:39] offset:64
	v_cvt_f32_f16_e32 v198, v240
	v_cvt_f32_f16_sdwa v199, v240 dst_sel:DWORD dst_unused:UNUSED_PAD src0_sel:WORD_1
	v_cvt_f32_f16_e32 v200, v241
	v_cvt_f32_f16_sdwa v201, v241 dst_sel:DWORD dst_unused:UNUSED_PAD src0_sel:WORD_1
	v_pk_fma_f32 v[192:193], v[190:191], v[108:109], v[124:125] op_sel_hi:[0,1,1]
	v_pk_fma_f32 v[194:195], v[190:191], v[110:111], v[126:127] op_sel_hi:[0,1,1]
	v_pk_mul_f32 v[192:193], v[192:193], s[46:47] op_sel:[0,1] op_sel_hi:[1,1]
	v_pk_mul_f32 v[194:195], v[194:195], s[46:47] op_sel:[0,1] op_sel_hi:[1,1]
	v_pk_fma_f32 v[192:193], s[46:47], v[140:141], v[192:193] op_sel_hi:[0,1,1]
	v_pk_fma_f32 v[194:195], s[46:47], v[142:143], v[194:195] op_sel_hi:[0,1,1]
	v_pk_mul_f32 v[192:193], v[192:193], v[198:199]
	v_pk_mul_f32 v[194:195], v[194:195], v[200:201]
	v_pk_fma_f32 v[250:251], v[192:193], v[192:193], v[250:251]
	v_pk_fma_f32 v[250:251], v[194:195], v[194:195], v[250:251]
	v_cvt_pk_f16_f32 v196, v192, v193
	v_cvt_pk_f16_f32 v197, v194, v195
	global_store_dwordx2 v242, v[196:197], s[38:39] offset:96
	s_add_u32 s38, s38, 0x80
	s_addc_u32 s39, s39, 0
	s_waitcnt vmcnt(15)
	s_waitcnt lgkmcnt(0)
	s_barrier
	ds_read_b128 v[144:147], v16 offset:16384
	ds_read_b128 v[148:151], v16 offset:20480
	ds_read_b128 v[152:155], v16 offset:24576
	ds_read_b128 v[156:159], v16 offset:28672
	ds_read_b32 v189, v36 offset:49152
	ds_read_b128 v[160:163], v17 offset:16384
	ds_read_b128 v[164:167], v17 offset:20480
	ds_read_b128 v[168:171], v17 offset:24576
	ds_read_b128 v[172:175], v17 offset:28672
	s_waitcnt lgkmcnt(4)
	v_mfma_f32_16x16x32_f16 v[96:99], v[144:147], v[44:47], 0
	v_mfma_f32_16x16x32_f16 v[100:103], v[148:151], v[44:47], 0
	v_mfma_f32_16x16x32_f16 v[104:107], v[152:155], v[44:47], 0
	v_mfma_f32_16x16x32_f16 v[108:111], v[156:159], v[44:47], 0
	ds_read_b128 v[144:147], v18 offset:16384
	ds_read_b128 v[148:151], v18 offset:20480
	ds_read_b128 v[152:155], v18 offset:24576
	ds_read_b128 v[156:159], v18 offset:28672
	s_waitcnt lgkmcnt(4)
	v_mfma_f32_16x16x32_f16 v[96:99], v[160:163], v[48:51], v[96:99]
	v_mfma_f32_16x16x32_f16 v[100:103], v[164:167], v[48:51], v[100:103]
	v_mfma_f32_16x16x32_f16 v[104:107], v[168:171], v[48:51], v[104:107]
	v_mfma_f32_16x16x32_f16 v[108:111], v[172:175], v[48:51], v[108:111]
	ds_read_b128 v[160:163], v19 offset:16384
	ds_read_b128 v[164:167], v19 offset:20480
	ds_read_b128 v[168:171], v19 offset:24576
	ds_read_b128 v[172:175], v19 offset:28672
	s_waitcnt lgkmcnt(4)
	v_mfma_f32_16x16x32_f16 v[96:99], v[144:147], v[52:55], v[96:99]
	v_mfma_f32_16x16x32_f16 v[100:103], v[148:151], v[52:55], v[100:103]
	v_mfma_f32_16x16x32_f16 v[104:107], v[152:155], v[52:55], v[104:107]
	v_mfma_f32_16x16x32_f16 v[108:111], v[156:159], v[52:55], v[108:111]
	ds_read_b128 v[176:179], v38 offset:49664
	ds_read_b128 v[180:183], v38 offset:49680
	ds_read_b32 v188, v38 offset:49152
	ds_read_b128 v[144:147], v16 offset:0
	ds_read_b128 v[148:151], v16 offset:4096
	ds_read_b128 v[152:155], v16 offset:8192
	ds_read_b128 v[156:159], v16 offset:12288
	s_waitcnt lgkmcnt(7)
	v_mfma_f32_16x16x32_f16 v[96:99], v[160:163], v[56:59], v[96:99]
	v_mfma_f32_16x16x32_f16 v[100:103], v[164:167], v[56:59], v[100:103]
	v_mfma_f32_16x16x32_f16 v[104:107], v[168:171], v[56:59], v[104:107]
	v_mfma_f32_16x16x32_f16 v[108:111], v[172:175], v[56:59], v[108:111]
	v_mul_f32_e32 v189, 0x3fb8aa3b, v189
	s_cmp_lt_u32 s42, 0
	s_cbranch_scc1 .Lmy_s2_kend55
	s_cmp_eq_u32 s42, 0
	s_cbranch_scc1 .Lmy_s2_diag56
	ds_read_b128 v[224:227], v38 offset:49792
	ds_read_b128 v[228:231], v38 offset:49808
	ds_read_b32 v232, v38 offset:49280
	ds_read_b128 v[160:163], v17 offset:0
	ds_read_b128 v[164:167], v17 offset:4096
	ds_read_b128 v[168:171], v17 offset:8192
	ds_read_b128 v[172:175], v17 offset:12288
	s_waitcnt lgkmcnt(7)
	v_fma_f32 v188, v188, s51, v189
	v_exp_f32_e32 v188, v188
	s_nop 0
	v_pk_mul_f32 v[176:177], v[176:177], v[188:189] op_sel_hi:[1,0]
	v_pk_mul_f32 v[178:179], v[178:179], v[188:189] op_sel_hi:[1,0]
	v_pk_mul_f32 v[180:181], v[180:181], v[188:189] op_sel_hi:[1,0]
	v_pk_mul_f32 v[182:183], v[182:183], v[188:189] op_sel_hi:[1,0]
	v_pk_mul_f32 v[176:177], v[60:61], v[176:177]
	v_pk_mul_f32 v[178:179], v[62:63], v[178:179]
	v_pk_mul_f32 v[180:181], v[64:65], v[180:181]
	v_pk_mul_f32 v[182:183], v[66:67], v[182:183]
	v_cvt_pk_f16_f32 v184, v176, v177
	v_cvt_pk_f16_f32 v185, v178, v179
	v_cvt_pk_f16_f32 v186, v180, v181
	v_cvt_pk_f16_f32 v187, v182, v183
	s_nop 1
	v_mfma_f32_16x16x32_f16 v[112:115], v[144:147], v[184:187], 0
	v_mfma_f32_16x16x32_f16 v[116:119], v[148:151], v[184:187], 0
	v_mfma_f32_16x16x32_f16 v[120:123], v[152:155], v[184:187], 0
	v_mfma_f32_16x16x32_f16 v[124:127], v[156:159], v[184:187], 0
	s_branch .Lmy_s2_knext57

.Lmy_s2_knext63:
.Lmy_s2_kend55:
	v_readlane_b32 s46, v11, 6
	v_readlane_b32 s47, v12, 6
	v_exp_f32_e32 v190, v189
	s_waitcnt lgkmcnt(0)
	s_nop 7
	v_cvt_f32_f16_e32 v198, v234
	v_cvt_f32_f16_sdwa v199, v234 dst_sel:DWORD dst_unused:UNUSED_PAD src0_sel:WORD_1
	v_cvt_f32_f16_e32 v200, v235
	v_cvt_f32_f16_sdwa v201, v235 dst_sel:DWORD dst_unused:UNUSED_PAD src0_sel:WORD_1
	v_pk_fma_f32 v[192:193], v[190:191], v[96:97], v[112:113] op_sel_hi:[0,1,1]
	v_pk_fma_f32 v[194:195], v[190:191], v[98:99], v[114:115] op_sel_hi:[0,1,1]
	v_pk_mul_f32 v[192:193], v[192:193], s[46:47] op_sel:[0,1] op_sel_hi:[1,1]
	v_pk_mul_f32 v[194:195], v[194:195], s[46:47] op_sel:[0,1] op_sel_hi:[1,1]
	v_pk_fma_f32 v[192:193], s[46:47], v[128:129], v[192:193] op_sel_hi:[0,1,1]
	v_pk_fma_f32 v[194:195], s[46:47], v[130:131], v[194:195] op_sel_hi:[0,1,1]
	v_pk_mul_f32 v[192:193], v[192:193], v[198:199]
	v_pk_mul_f32 v[194:195], v[194:195], v[200:201]
	v_pk_fma_f32 v[250:251], v[192:193], v[192:193], v[250:251]
	v_pk_fma_f32 v[250:251], v[194:195], v[194:195], v[250:251]
	v_cvt_pk_f16_f32 v196, v192, v193
	v_cvt_pk_f16_f32 v197, v194, v195
	global_store_dwordx2 v242, v[196:197], s[38:39]
	v_cvt_f32_f16_e32 v198, v236
	v_cvt_f32_f16_sdwa v199, v236 dst_sel:DWORD dst_unused:UNUSED_PAD src0_sel:WORD_1
	v_cvt_f32_f16_e32 v200, v237
	v_cvt_f32_f16_sdwa v201, v237 dst_sel:DWORD dst_unused:UNUSED_PAD src0_sel:WORD_1
	v_pk_fma_f32 v[192:193], v[190:191], v[100:101], v[116:117] op_sel_hi:[0,1,1]
	v_pk_fma_f32 v[194:195], v[190:191], v[102:103], v[118:119] op_sel_hi:[0,1,1]
	v_pk_mul_f32 v[192:193], v[192:193], s[46:47] op_sel:[0,1] op_sel_hi:[1,1]
	v_pk_mul_f32 v[194:195], v[194:195], s[46:47] op_sel:[0,1] op_sel_hi:[1,1]
	v_pk_fma_f32 v[192:193], s[46:47], v[132:133], v[192:193] op_sel_hi:[0,1,1]
	v_pk_fma_f32 v[194:195], s[46:47], v[134:135], v[194:195] op_sel_hi:[0,1,1]
	v_pk_mul_f32 v[192:193], v[192:193], v[198:199]
	v_pk_mul_f32 v[194:195], v[194:195], v[200:201]
	v_pk_fma_f32 v[250:251], v[192:193], v[192:193], v[250:251]
	v_pk_fma_f32 v[250:251], v[194:195], v[194:195], v[250:251]
	v_cvt_pk_f16_f32 v196, v192, v193
	v_cvt_pk_f16_f32 v197, v194, v195
	global_store_dwordx2 v242, v[196:197], s[38:39] offset:32
	v_cvt_f32_f16_e32 v198, v238
	v_cvt_f32_f16_sdwa v199, v238 dst_sel:DWORD dst_unused:UNUSED_PAD src0_sel:WORD_1
	v_cvt_f32_f16_e32 v200, v239
	v_cvt_f32_f16_sdwa v201, v239 dst_sel:DWORD dst_unused:UNUSED_PAD src0_sel:WORD_1
	v_pk_fma_f32 v[192:193], v[190:191], v[104:105], v[120:121] op_sel_hi:[0,1,1]
	v_pk_fma_f32 v[194:195], v[190:191], v[106:107], v[122:123] op_sel_hi:[0,1,1]
	v_pk_mul_f32 v[192:193], v[192:193], s[46:47] op_sel:[0,1] op_sel_hi:[1,1]
	v_pk_mul_f32 v[194:195], v[194:195], s[46:47] op_sel:[0,1] op_sel_hi:[1,1]
	v_pk_fma_f32 v[192:193], s[46:47], v[136:137], v[192:193] op_sel_hi:[0,1,1]
	v_pk_fma_f32 v[194:195], s[46:47], v[138:139], v[194:195] op_sel_hi:[0,1,1]
	v_pk_mul_f32 v[192:193], v[192:193], v[198:199]
	v_pk_mul_f32 v[194:195], v[194:195], v[200:201]
	v_pk_fma_f32 v[250:251], v[192:193], v[192:193], v[250:251]
	v_pk_fma_f32 v[250:251], v[194:195], v[194:195], v[250:251]
	v_cvt_pk_f16_f32 v196, v192, v193
	v_cvt_pk_f16_f32 v197, v194, v195
	global_store_dwordx2 v242, v[196:197], s[38:39] offset:64
	v_cvt_f32_f16_e32 v198, v240
	v_cvt_f32_f16_sdwa v199, v240 dst_sel:DWORD dst_unused:UNUSED_PAD src0_sel:WORD_1
	v_cvt_f32_f16_e32 v200, v241
	v_cvt_f32_f16_sdwa v201, v241 dst_sel:DWORD dst_unused:UNUSED_PAD src0_sel:WORD_1
	v_pk_fma_f32 v[192:193], v[190:191], v[108:109], v[124:125] op_sel_hi:[0,1,1]
	v_pk_fma_f32 v[194:195], v[190:191], v[110:111], v[126:127] op_sel_hi:[0,1,1]
	v_pk_mul_f32 v[192:193], v[192:193], s[46:47] op_sel:[0,1] op_sel_hi:[1,1]
	v_pk_mul_f32 v[194:195], v[194:195], s[46:47] op_sel:[0,1] op_sel_hi:[1,1]
	v_pk_fma_f32 v[192:193], s[46:47], v[140:141], v[192:193] op_sel_hi:[0,1,1]
	v_pk_fma_f32 v[194:195], s[46:47], v[142:143], v[194:195] op_sel_hi:[0,1,1]
	v_pk_mul_f32 v[192:193], v[192:193], v[198:199]
	v_pk_mul_f32 v[194:195], v[194:195], v[200:201]
	v_pk_fma_f32 v[250:251], v[192:193], v[192:193], v[250:251]
	v_pk_fma_f32 v[250:251], v[194:195], v[194:195], v[250:251]
	v_cvt_pk_f16_f32 v196, v192, v193
	v_cvt_pk_f16_f32 v197, v194, v195
	global_store_dwordx2 v242, v[196:197], s[38:39] offset:96
	s_add_u32 s38, s38, 0x80
	s_addc_u32 s39, s39, 0
	s_waitcnt vmcnt(8)
	s_waitcnt lgkmcnt(0)
	s_barrier
	ds_read_b128 v[144:147], v20 offset:16384
	ds_read_b128 v[148:151], v20 offset:20480
	ds_read_b128 v[152:155], v20 offset:24576
	ds_read_b128 v[156:159], v20 offset:28672
	ds_read_b32 v189, v37 offset:49152
	ds_read_b128 v[160:163], v21 offset:16384
	ds_read_b128 v[164:167], v21 offset:20480
	ds_read_b128 v[168:171], v21 offset:24576
	ds_read_b128 v[172:175], v21 offset:28672
	s_waitcnt lgkmcnt(4)
	v_mfma_f32_16x16x32_f16 v[96:99], v[144:147], v[44:47], 0
	v_mfma_f32_16x16x32_f16 v[100:103], v[148:151], v[44:47], 0
	v_mfma_f32_16x16x32_f16 v[104:107], v[152:155], v[44:47], 0
	v_mfma_f32_16x16x32_f16 v[108:111], v[156:159], v[44:47], 0
	ds_read_b128 v[144:147], v22 offset:16384
	ds_read_b128 v[148:151], v22 offset:20480
	ds_read_b128 v[152:155], v22 offset:24576
	ds_read_b128 v[156:159], v22 offset:28672
	s_waitcnt lgkmcnt(4)
	v_mfma_f32_16x16x32_f16 v[96:99], v[160:163], v[48:51], v[96:99]
	v_mfma_f32_16x16x32_f16 v[100:103], v[164:167], v[48:51], v[100:103]
	v_mfma_f32_16x16x32_f16 v[104:107], v[168:171], v[48:51], v[104:107]
	v_mfma_f32_16x16x32_f16 v[108:111], v[172:175], v[48:51], v[108:111]
	ds_read_b128 v[160:163], v23 offset:16384
	ds_read_b128 v[164:167], v23 offset:20480
	ds_read_b128 v[168:171], v23 offset:24576
	ds_read_b128 v[172:175], v23 offset:28672
	s_waitcnt lgkmcnt(4)
	v_mfma_f32_16x16x32_f16 v[96:99], v[144:147], v[52:55], v[96:99]
	v_mfma_f32_16x16x32_f16 v[100:103], v[148:151], v[52:55], v[100:103]
	v_mfma_f32_16x16x32_f16 v[104:107], v[152:155], v[52:55], v[104:107]
	v_mfma_f32_16x16x32_f16 v[108:111], v[156:159], v[52:55], v[108:111]
	ds_read_b128 v[176:179], v39 offset:49664
	ds_read_b128 v[180:183], v39 offset:49680
	ds_read_b32 v188, v39 offset:49152
	ds_read_b128 v[144:147], v20 offset:0
	ds_read_b128 v[148:151], v20 offset:4096
	ds_read_b128 v[152:155], v20 offset:8192
	ds_read_b128 v[156:159], v20 offset:12288
	s_waitcnt lgkmcnt(7)
	v_mfma_f32_16x16x32_f16 v[96:99], v[160:163], v[56:59], v[96:99]
	v_mfma_f32_16x16x32_f16 v[100:103], v[164:167], v[56:59], v[100:103]
	v_mfma_f32_16x16x32_f16 v[104:107], v[168:171], v[56:59], v[104:107]
	v_mfma_f32_16x16x32_f16 v[108:111], v[172:175], v[56:59], v[108:111]
	v_mul_f32_e32 v189, 0x3fb8aa3b, v189
	s_cmp_lt_u32 s42, 0
	s_cbranch_scc1 .Lmy_s2_kend64
	s_cmp_eq_u32 s42, 0
	s_cbranch_scc1 .Lmy_s2_diag65
	ds_read_b128 v[224:227], v39 offset:49792
	ds_read_b128 v[228:231], v39 offset:49808
	ds_read_b32 v232, v39 offset:49280
	ds_read_b128 v[160:163], v21 offset:0
	ds_read_b128 v[164:167], v21 offset:4096
	ds_read_b128 v[168:171], v21 offset:8192
	ds_read_b128 v[172:175], v21 offset:12288
	s_waitcnt lgkmcnt(7)
	v_fma_f32 v188, v188, s51, v189
	v_exp_f32_e32 v188, v188
	s_nop 0
	v_pk_mul_f32 v[176:177], v[176:177], v[188:189] op_sel_hi:[1,0]
	v_pk_mul_f32 v[178:179], v[178:179], v[188:189] op_sel_hi:[1,0]
	v_pk_mul_f32 v[180:181], v[180:181], v[188:189] op_sel_hi:[1,0]
	v_pk_mul_f32 v[182:183], v[182:183], v[188:189] op_sel_hi:[1,0]
	v_pk_mul_f32 v[176:177], v[60:61], v[176:177]
	v_pk_mul_f32 v[178:179], v[62:63], v[178:179]
	v_pk_mul_f32 v[180:181], v[64:65], v[180:181]
	v_pk_mul_f32 v[182:183], v[66:67], v[182:183]
	v_cvt_pk_f16_f32 v184, v176, v177
	v_cvt_pk_f16_f32 v185, v178, v179
	v_cvt_pk_f16_f32 v186, v180, v181
	v_cvt_pk_f16_f32 v187, v182, v183
	s_nop 1
	v_mfma_f32_16x16x32_f16 v[112:115], v[144:147], v[184:187], 0
	v_mfma_f32_16x16x32_f16 v[116:119], v[148:151], v[184:187], 0
	v_mfma_f32_16x16x32_f16 v[120:123], v[152:155], v[184:187], 0
	v_mfma_f32_16x16x32_f16 v[124:127], v[156:159], v[184:187], 0
	s_branch .Lmy_s2_knext66

.Lmy_s2_knext72:
.Lmy_s2_kend64:
	v_readlane_b32 s46, v11, 7
	v_readlane_b32 s47, v12, 7
	v_exp_f32_e32 v190, v189
	s_waitcnt lgkmcnt(0)
	s_nop 7
	v_cvt_f32_f16_e32 v198, v234
	v_cvt_f32_f16_sdwa v199, v234 dst_sel:DWORD dst_unused:UNUSED_PAD src0_sel:WORD_1
	v_cvt_f32_f16_e32 v200, v235
	v_cvt_f32_f16_sdwa v201, v235 dst_sel:DWORD dst_unused:UNUSED_PAD src0_sel:WORD_1
	v_pk_fma_f32 v[192:193], v[190:191], v[96:97], v[112:113] op_sel_hi:[0,1,1]
	v_pk_fma_f32 v[194:195], v[190:191], v[98:99], v[114:115] op_sel_hi:[0,1,1]
	v_pk_mul_f32 v[192:193], v[192:193], s[46:47] op_sel:[0,1] op_sel_hi:[1,1]
	v_pk_mul_f32 v[194:195], v[194:195], s[46:47] op_sel:[0,1] op_sel_hi:[1,1]
	v_pk_fma_f32 v[192:193], s[46:47], v[128:129], v[192:193] op_sel_hi:[0,1,1]
	v_pk_fma_f32 v[194:195], s[46:47], v[130:131], v[194:195] op_sel_hi:[0,1,1]
	v_pk_mul_f32 v[192:193], v[192:193], v[198:199]
	v_pk_mul_f32 v[194:195], v[194:195], v[200:201]
	v_pk_fma_f32 v[250:251], v[192:193], v[192:193], v[250:251]
	v_pk_fma_f32 v[250:251], v[194:195], v[194:195], v[250:251]
	v_cvt_pk_f16_f32 v196, v192, v193
	v_cvt_pk_f16_f32 v197, v194, v195
	global_store_dwordx2 v242, v[196:197], s[38:39]
	v_cvt_f32_f16_e32 v198, v236
	v_cvt_f32_f16_sdwa v199, v236 dst_sel:DWORD dst_unused:UNUSED_PAD src0_sel:WORD_1
	v_cvt_f32_f16_e32 v200, v237
	v_cvt_f32_f16_sdwa v201, v237 dst_sel:DWORD dst_unused:UNUSED_PAD src0_sel:WORD_1
	v_pk_fma_f32 v[192:193], v[190:191], v[100:101], v[116:117] op_sel_hi:[0,1,1]
	v_pk_fma_f32 v[194:195], v[190:191], v[102:103], v[118:119] op_sel_hi:[0,1,1]
	v_pk_mul_f32 v[192:193], v[192:193], s[46:47] op_sel:[0,1] op_sel_hi:[1,1]
	v_pk_mul_f32 v[194:195], v[194:195], s[46:47] op_sel:[0,1] op_sel_hi:[1,1]
	v_pk_fma_f32 v[192:193], s[46:47], v[132:133], v[192:193] op_sel_hi:[0,1,1]
	v_pk_fma_f32 v[194:195], s[46:47], v[134:135], v[194:195] op_sel_hi:[0,1,1]
	v_pk_mul_f32 v[192:193], v[192:193], v[198:199]
	v_pk_mul_f32 v[194:195], v[194:195], v[200:201]
	v_pk_fma_f32 v[250:251], v[192:193], v[192:193], v[250:251]
	v_pk_fma_f32 v[250:251], v[194:195], v[194:195], v[250:251]
	v_cvt_pk_f16_f32 v196, v192, v193
	v_cvt_pk_f16_f32 v197, v194, v195
	global_store_dwordx2 v242, v[196:197], s[38:39] offset:32
	v_cvt_f32_f16_e32 v198, v238
	v_cvt_f32_f16_sdwa v199, v238 dst_sel:DWORD dst_unused:UNUSED_PAD src0_sel:WORD_1
	v_cvt_f32_f16_e32 v200, v239
	v_cvt_f32_f16_sdwa v201, v239 dst_sel:DWORD dst_unused:UNUSED_PAD src0_sel:WORD_1
	v_pk_fma_f32 v[192:193], v[190:191], v[104:105], v[120:121] op_sel_hi:[0,1,1]
	v_pk_fma_f32 v[194:195], v[190:191], v[106:107], v[122:123] op_sel_hi:[0,1,1]
	v_pk_mul_f32 v[192:193], v[192:193], s[46:47] op_sel:[0,1] op_sel_hi:[1,1]
	v_pk_mul_f32 v[194:195], v[194:195], s[46:47] op_sel:[0,1] op_sel_hi:[1,1]
	v_pk_fma_f32 v[192:193], s[46:47], v[136:137], v[192:193] op_sel_hi:[0,1,1]
	v_pk_fma_f32 v[194:195], s[46:47], v[138:139], v[194:195] op_sel_hi:[0,1,1]
	v_pk_mul_f32 v[192:193], v[192:193], v[198:199]
	v_pk_mul_f32 v[194:195], v[194:195], v[200:201]
	v_pk_fma_f32 v[250:251], v[192:193], v[192:193], v[250:251]
	v_pk_fma_f32 v[250:251], v[194:195], v[194:195], v[250:251]
	v_cvt_pk_f16_f32 v196, v192, v193
	v_cvt_pk_f16_f32 v197, v194, v195
	global_store_dwordx2 v242, v[196:197], s[38:39] offset:64
	v_cvt_f32_f16_e32 v198, v240
	v_cvt_f32_f16_sdwa v199, v240 dst_sel:DWORD dst_unused:UNUSED_PAD src0_sel:WORD_1
	v_cvt_f32_f16_e32 v200, v241
	v_cvt_f32_f16_sdwa v201, v241 dst_sel:DWORD dst_unused:UNUSED_PAD src0_sel:WORD_1
	v_pk_fma_f32 v[192:193], v[190:191], v[108:109], v[124:125] op_sel_hi:[0,1,1]
	v_pk_fma_f32 v[194:195], v[190:191], v[110:111], v[126:127] op_sel_hi:[0,1,1]
	v_pk_mul_f32 v[192:193], v[192:193], s[46:47] op_sel:[0,1] op_sel_hi:[1,1]
	v_pk_mul_f32 v[194:195], v[194:195], s[46:47] op_sel:[0,1] op_sel_hi:[1,1]
	v_pk_fma_f32 v[192:193], s[46:47], v[140:141], v[192:193] op_sel_hi:[0,1,1]
	v_pk_fma_f32 v[194:195], s[46:47], v[142:143], v[194:195] op_sel_hi:[0,1,1]
	v_pk_mul_f32 v[192:193], v[192:193], v[198:199]
	v_pk_mul_f32 v[194:195], v[194:195], v[200:201]
	v_pk_fma_f32 v[250:251], v[192:193], v[192:193], v[250:251]
	v_pk_fma_f32 v[250:251], v[194:195], v[194:195], v[250:251]
	v_cvt_pk_f16_f32 v196, v192, v193
	v_cvt_pk_f16_f32 v197, v194, v195
	global_store_dwordx2 v242, v[196:197], s[38:39] offset:96
	s_add_u32 s38, s38, 0x80
	s_addc_u32 s39, s39, 0
	v_add_f32_e32 v13, v250, v251
	v_mul_f32_e32 v13, 0x3b800000, v13
	v_mbcnt_lo_u32_b32 v188, -1, 0
	v_mbcnt_hi_u32_b32 v188, -1, v188
	v_xor_b32_e32 v189, 16, v188
	v_lshlrev_b32_e32 v189, 2, v189
	ds_bpermute_b32 v190, v189, v13
	s_waitcnt lgkmcnt(0)
	v_add_f32_e32 v13, v13, v190
	v_xor_b32_e32 v189, 32, v188
	v_lshlrev_b32_e32 v189, 2, v189
	ds_bpermute_b32 v190, v189, v13
	s_waitcnt lgkmcnt(0)
	v_add_f32_e32 v13, v13, v190
	v_cmp_gt_u32_e32 vcc, 16, v188
	s_and_saveexec_b64 s[48:49], vcc
	s_cbranch_execz .Lmy_s2_noat73
	global_atomic_add_f32 v15, v13, s[24:25]

	.amdhsa_kernel _Z12scan2_kernelPKDF16_S0_S0_S0_S0_PKfS2_S2_S2_PDF16_PfS4_
		.amdhsa_group_segment_fixed_size 34816
		.amdhsa_private_segment_fixed_size 0
		.amdhsa_kernarg_size 96
		.amdhsa_user_sgpr_count 2
		.amdhsa_user_sgpr_dispatch_ptr 0
		.amdhsa_user_sgpr_queue_ptr 0
		.amdhsa_user_sgpr_kernarg_segment_ptr 1
		.amdhsa_user_sgpr_dispatch_id 0
		.amdhsa_user_sgpr_kernarg_preload_length 0
		.amdhsa_user_sgpr_kernarg_preload_offset 0
		.amdhsa_user_sgpr_private_segment_size 0
		.amdhsa_uses_dynamic_stack 0
		.amdhsa_enable_private_segment 0
		.amdhsa_system_sgpr_workgroup_id_x 1
		.amdhsa_system_sgpr_workgroup_id_y 0
		.amdhsa_system_sgpr_workgroup_id_z 0
		.amdhsa_system_sgpr_workgroup_info 0
		.amdhsa_system_vgpr_workitem_id 0
		.amdhsa_next_free_vgpr 252
		.amdhsa_next_free_sgpr 68
		.amdhsa_accum_offset 252
		.amdhsa_reserve_vcc 1
		.amdhsa_float_round_mode_32 0
		.amdhsa_float_round_mode_16_64 0
		.amdhsa_float_denorm_mode_32 3
		.amdhsa_float_denorm_mode_16_64 3
		.amdhsa_dx10_clamp 1
		.amdhsa_ieee_mode 1
		.amdhsa_fp16_overflow 0
		.amdhsa_tg_split 0
		.amdhsa_exception_fp_ieee_invalid_op 0
		.amdhsa_exception_fp_denorm_src 0
		.amdhsa_exception_fp_ieee_div_zero 0
		.amdhsa_exception_fp_ieee_overflow 0
		.amdhsa_exception_fp_ieee_underflow 0
		.amdhsa_exception_fp_ieee_inexact 0
		.amdhsa_exception_int_div_zero 0
	.end_amdhsa_kernel

amdhsa.kernels:
  - .agpr_count:     0
    .args:
      - .actual_access:  read_only
        .address_space:  global
        .offset:         0
        .size:           8
        .value_kind:     global_buffer
      - .actual_access:  read_only
        .address_space:  global
        .offset:         8
        .size:           8
        .value_kind:     global_buffer
      - .actual_access:  read_only
        .address_space:  global
        .offset:         16
        .size:           8
        .value_kind:     global_buffer
      - .actual_access:  read_only
        .address_space:  global
        .offset:         24
        .size:           8
        .value_kind:     global_buffer
      - .actual_access:  write_only
        .address_space:  global
        .offset:         32
        .size:           8
        .value_kind:     global_buffer
      - .actual_access:  write_only
        .address_space:  global
        .offset:         40
        .size:           8
        .value_kind:     global_buffer
      - .actual_access:  write_only
        .address_space:  global
        .offset:         48
        .size:           8
        .value_kind:     global_buffer
      - .actual_access:  write_only
        .address_space:  global
        .offset:         56
        .size:           8
        .value_kind:     global_buffer
    .group_segment_fixed_size: 16640
    .kernarg_segment_align: 8
    .kernarg_segment_size: 64
    .language:       OpenCL C
    .language_version:
      - 2
      - 0
    .max_flat_workgroup_size: 256
    .name:           _Z11prep_kernelPKfS0_S0_S0_PDF16_S1_S1_Pf
    .private_segment_fixed_size: 0
    .sgpr_count:     18
    .sgpr_spill_count: 0
    .symbol:         _Z11prep_kernelPKfS0_S0_S0_PDF16_S1_S1_Pf.kd
    .uniform_work_group_size: 1
    .uses_dynamic_stack: false
    .vgpr_count:     42
    .vgpr_spill_count: 0
    .wavefront_size: 64
  - .agpr_count:     0
    .args:
      - .address_space:  global
        .offset:         0
        .size:           8
        .value_kind:     global_buffer
      - .address_space:  global
        .offset:         8
        .size:           8
        .value_kind:     global_buffer
      - .actual_access:  write_only
        .address_space:  global
        .offset:         16
        .size:           8
        .value_kind:     global_buffer
      - .actual_access:  read_only
        .address_space:  global
        .offset:         24
        .size:           8
        .value_kind:     global_buffer
    .group_segment_fixed_size: 49152
    .kernarg_segment_align: 8
    .kernarg_segment_size: 32
    .language:       OpenCL C
    .language_version:
      - 2
      - 0
    .max_flat_workgroup_size: 512
    .name:           _Z13gemm2b_kernelPKDF16_S0_PfPKf
    .private_segment_fixed_size: 0
    .sgpr_count:     24
    .sgpr_spill_count: 0
    .symbol:         _Z13gemm2b_kernelPKDF16_S0_PfPKf.kd
    .uniform_work_group_size: 1
    .uses_dynamic_stack: false
    .vgpr_count:     176
    .vgpr_spill_count: 0
    .wavefront_size: 64
  - .agpr_count:     0
    .args:
      - .address_space:  global
        .offset:         0
        .size:           8
        .value_kind:     global_buffer
      - .address_space:  global
        .offset:         8
        .size:           8
        .value_kind:     global_buffer
      - .actual_access:  write_only
        .address_space:  global
        .offset:         16
        .size:           8
        .value_kind:     global_buffer
      - .actual_access:  write_only
        .address_space:  global
        .offset:         24
        .size:           8
        .value_kind:     global_buffer
    .group_segment_fixed_size: 16384
    .kernarg_segment_align: 8
    .kernarg_segment_size: 32
    .language:       OpenCL C
    .language_version:
      - 2
      - 0
    .max_flat_workgroup_size: 512
    .name:           _Z12gemm8_kernelPKDF16_S0_PDF16_S1_
    .private_segment_fixed_size: 0
    .sgpr_count:     58
    .sgpr_spill_count: 0
    .symbol:         _Z12gemm8_kernelPKDF16_S0_PDF16_S1_.kd
    .uniform_work_group_size: 1
    .uses_dynamic_stack: false
    .vgpr_count:     184
    .vgpr_spill_count: 0
    .wavefront_size: 64
  - .agpr_count:     0
    .args:
      - .actual_access:  read_only
        .address_space:  global
        .offset:         0
        .size:           8
        .value_kind:     global_buffer
      - .actual_access:  read_only
        .address_space:  global
        .offset:         8
        .size:           8
        .value_kind:     global_buffer
      - .actual_access:  read_only
        .address_space:  global
        .offset:         16
        .size:           8
        .value_kind:     global_buffer
      - .actual_access:  read_only
        .address_space:  global
        .offset:         24
        .size:           8
        .value_kind:     global_buffer
      - .actual_access:  write_only
        .address_space:  global
        .offset:         32
        .size:           8
        .value_kind:     global_buffer
      - .actual_access:  write_only
        .address_space:  global
        .offset:         40
        .size:           8
        .value_kind:     global_buffer
      - .actual_access:  read_only
        .address_space:  global
        .offset:         48
        .size:           8
        .value_kind:     global_buffer
      - .actual_access:  read_only
        .address_space:  global
        .offset:         56
        .size:           8
        .value_kind:     global_buffer
      - .actual_access:  read_only
        .address_space:  global
        .offset:         64
        .size:           8
        .value_kind:     global_buffer
      - .actual_access:  write_only
        .address_space:  global
        .offset:         72
        .size:           8
        .value_kind:     global_buffer
      - .actual_access:  write_only
        .address_space:  global
        .offset:         80
        .size:           8
        .value_kind:     global_buffer
      - .actual_access:  write_only
        .address_space:  global
        .offset:         88
        .size:           8
        .value_kind:     global_buffer
      - .actual_access:  write_only
        .address_space:  global
        .offset:         96
        .size:           8
        .value_kind:     global_buffer
    .group_segment_fixed_size: 17952
    .kernarg_segment_align: 8
    .kernarg_segment_size: 104
    .language:       OpenCL C
    .language_version:
      - 2
      - 0
    .max_flat_workgroup_size: 256
    .name:           _Z13convdt_kernelPKDF16_S0_PKfS2_PDF16_S3_S2_S2_S2_PfS4_S4_S4_
    .private_segment_fixed_size: 0
    .sgpr_count:     26
    .sgpr_spill_count: 0
    .symbol:         _Z13convdt_kernelPKDF16_S0_PKfS2_PDF16_S3_S2_S2_S2_PfS4_S4_S4_.kd
    .uniform_work_group_size: 1
    .uses_dynamic_stack: false
    .vgpr_count:     88
    .vgpr_spill_count: 0
    .wavefront_size: 64
  - .agpr_count:     0
    .args:
      - .actual_access:  read_only
        .address_space:  global
        .offset:         0
        .size:           8
        .value_kind:     global_buffer
      - .actual_access:  read_only
        .address_space:  global
        .offset:         8
        .size:           8
        .value_kind:     global_buffer
      - .actual_access:  read_only
        .address_space:  global
        .offset:         16
        .size:           8
        .value_kind:     global_buffer
      - .actual_access:  write_only
        .address_space:  global
        .offset:         24
        .size:           8
        .value_kind:     global_buffer
    .group_segment_fixed_size: 34816
    .kernarg_segment_align: 8
    .kernarg_segment_size: 32
    .language:       OpenCL C
    .language_version:
      - 2
      - 0
    .max_flat_workgroup_size: 256
    .name:           _Z11sloc_kernelPKDF16_PKfS2_PDF16_
    .private_segment_fixed_size: 0
    .sgpr_count:     28
    .sgpr_spill_count: 0
    .symbol:         _Z11sloc_kernelPKDF16_PKfS2_PDF16_.kd
    .uniform_work_group_size: 1
    .uses_dynamic_stack: false
    .vgpr_count:     120
    .vgpr_spill_count: 0
    .wavefront_size: 64
  - .agpr_count:     64
    .args:
      - .actual_access:  read_only
        .address_space:  global
        .offset:         0
        .size:           8
        .value_kind:     global_buffer
      - .address_space:  global
        .offset:         8
        .size:           8
        .value_kind:     global_buffer
      - .actual_access:  read_only
        .address_space:  global
        .offset:         16
        .size:           8
        .value_kind:     global_buffer
      - .actual_access:  write_only
        .address_space:  global
        .offset:         24
        .size:           8
        .value_kind:     global_buffer
    .group_segment_fixed_size: 0
    .kernarg_segment_align: 8
    .kernarg_segment_size: 32
    .language:       OpenCL C
    .language_version:
      - 2
      - 0
    .max_flat_workgroup_size: 256
    .name:           _Z12spass_kernelPKfPDF16_PKDF16_S1_
    .private_segment_fixed_size: 0
    .sgpr_count:     21
    .sgpr_spill_count: 0
    .symbol:         _Z12spass_kernelPKfPDF16_PKDF16_S1_.kd
    .uniform_work_group_size: 1
    .uses_dynamic_stack: false
    .vgpr_count:     180
    .vgpr_spill_count: 0
    .wavefront_size: 64
  - .agpr_count:     0
    .args:
      - .actual_access:  read_only
        .address_space:  global
        .offset:         0
        .size:           8
        .value_kind:     global_buffer
      - .actual_access:  read_only
        .address_space:  global
        .offset:         8
        .size:           8
        .value_kind:     global_buffer
      - .actual_access:  read_only
        .address_space:  global
        .offset:         16
        .size:           8
        .value_kind:     global_buffer
      - .actual_access:  read_only
        .address_space:  global
        .offset:         24
        .size:           8
        .value_kind:     global_buffer
      - .actual_access:  read_only
        .address_space:  global
        .offset:         32
        .size:           8
        .value_kind:     global_buffer
      - .actual_access:  read_only
        .address_space:  global
        .offset:         40
        .size:           8
        .value_kind:     global_buffer
      - .actual_access:  read_only
        .address_space:  global
        .offset:         48
        .size:           8
        .value_kind:     global_buffer
      - .actual_access:  read_only
        .address_space:  global
        .offset:         56
        .size:           8
        .value_kind:     global_buffer
      - .actual_access:  read_only
        .address_space:  global
        .offset:         64
        .size:           8
        .value_kind:     global_buffer
      - .actual_access:  write_only
        .address_space:  global
        .offset:         72
        .size:           8
        .value_kind:     global_buffer
      - .address_space:  global
        .offset:         80
        .size:           8
        .value_kind:     global_buffer
      - .actual_access:  read_only
        .address_space:  global
        .offset:         88
        .size:           8
        .value_kind:     global_buffer
    .group_segment_fixed_size: 54272
    .kernarg_segment_align: 8
    .kernarg_segment_size: 96
    .language:       OpenCL C
    .language_version:
      - 2
      - 0
    .max_flat_workgroup_size: 256
    .name:           _Z11scan_kernelPKDF16_S0_S0_S0_S0_PKfS2_S2_S2_PDF16_PfS4_
    .private_segment_fixed_size: 0
    .sgpr_count:     106
    .sgpr_spill_count: 56
    .symbol:         _Z11scan_kernelPKDF16_S0_S0_S0_S0_PKfS2_S2_S2_PDF16_PfS4_.kd
    .uniform_work_group_size: 1
    .uses_dynamic_stack: false
    .vgpr_count:     243
    .vgpr_spill_count: 0
    .wavefront_size: 64
  - .agpr_count:     0
    .args:
      - .actual_access:  read_only
        .address_space:  global
        .offset:         0
        .size:           8
        .value_kind:     global_buffer
      - .address_space:  global
        .offset:         8
        .size:           8
        .value_kind:     global_buffer
      - .address_space:  global
        .offset:         16
        .size:           8
        .value_kind:     global_buffer
      - .actual_access:  read_only
        .address_space:  global
        .offset:         24
        .size:           8
        .value_kind:     global_buffer
      - .address_space:  global
        .offset:         32
        .size:           8
        .value_kind:     global_buffer
      - .address_space:  global
        .offset:         40
        .size:           8
        .value_kind:     global_buffer
      - .address_space:  global
        .offset:         48
        .size:           8
        .value_kind:     global_buffer
      - .actual_access:  read_only
        .address_space:  global
        .offset:         56
        .size:           8
        .value_kind:     global_buffer
      - .actual_access:  read_only
        .address_space:  global
        .offset:         64
        .size:           8
        .value_kind:     global_buffer
      - .actual_access:  write_only
        .address_space:  global
        .offset:         72
        .size:           8
        .value_kind:     global_buffer
      - .address_space:  global
        .offset:         80
        .size:           8
        .value_kind:     global_buffer
      - .actual_access:  read_only
        .address_space:  global
        .offset:         88
        .size:           8
        .value_kind:     global_buffer
    .group_segment_fixed_size: 34816
    .kernarg_segment_align: 8
    .kernarg_segment_size: 96
    .language:       OpenCL C
    .language_version:
      - 2
      - 0
    .max_flat_workgroup_size: 512
    .name:           _Z12scan2_kernelPKDF16_S0_S0_S0_S0_PKfS2_S2_S2_PDF16_PfS4_
    .private_segment_fixed_size: 0
    .sgpr_count:     74
    .sgpr_spill_count: 0
    .symbol:         _Z12scan2_kernelPKDF16_S0_S0_S0_S0_PKfS2_S2_S2_PDF16_PfS4_.kd
    .uniform_work_group_size: 1
    .uses_dynamic_stack: false
    .vgpr_count:     252
    .vgpr_spill_count: 0
    .wavefront_size: 64
  - .agpr_count:     64
    .args:
      - .address_space:  global
        .offset:         0
        .size:           8
        .value_kind:     global_buffer
      - .address_space:  global
        .offset:         8
        .size:           8
        .value_kind:     global_buffer
      - .offset:         16
        .size:           4
        .value_kind:     by_value
      - .offset:         20
        .size:           4
        .value_kind:     by_value
      - .offset:         24
        .size:           4
        .value_kind:     by_value
      - .actual_access:  write_only
        .address_space:  global
        .offset:         32
        .size:           8
        .value_kind:     global_buffer
      - .actual_access:  write_only
        .address_space:  global
        .offset:         40
        .size:           8
        .value_kind:     global_buffer
      - .actual_access:  read_only
        .address_space:  global
        .offset:         48
        .size:           8
        .value_kind:     global_buffer
      - .offset:         56
        .size:           4
        .value_kind:     by_value
    .group_segment_fixed_size: 131072
    .kernarg_segment_align: 8
    .kernarg_segment_size: 60
    .language:       OpenCL C
    .language_version:
      - 2
      - 0
    .max_flat_workgroup_size: 256
    .name:           _Z11gemm_kernelILi1EEvPKDF16_S1_iiiPDF16_PfPKfi
    .private_segment_fixed_size: 0
    .sgpr_count:     27
    .sgpr_spill_count: 0
    .symbol:         _Z11gemm_kernelILi1EEvPKDF16_S1_iiiPDF16_PfPKfi.kd
    .uniform_work_group_size: 1
    .uses_dynamic_stack: false
    .vgpr_count:     208
    .vgpr_spill_count: 0
    .wavefront_size: 64
